# GEMM K-loops (7): move As[0][0] stage (2 LDS-DMAs) from load segment 2 to segment 3 (2/6/2/6 -> 2/4/4/6), vmcnt waits 8/8/8/8 -> 8/6/8/6
# speedup vs baseline: 1.0061x; 1.0044x over previous
; #define PG8_STAGE(bufoff, gbase, voff) do { _Pragma("unroll") for (int _i = 0; _i < 2; ++_i) \
;         __builtin_amdgcn_global_load_lds((const unsigned*)((const char*)(gbase) + (voff)[_i]), (PG8_LAS unsigned*)(lds + (bufoff) + ldsw + _i * 8192), 16, 0, 0); } while (0)
; #define PG8_LDA(dst, b, h) do { _Pragma("unroll") for (int m = 0; m < 4; ++m) { const bf16x8 f0_ = *(const PG8_LAS bf16x8*)(lds + PG8_SA(b, h) + aoff + m * 2048), f1_ = *(const PG8_LAS bf16x8*)(lds + PG8_SA(b, h) + aoff + m * 2048 + 1024); dst[m].set(f0_, f1_); } } while (0)
; #define PG8_LDB(dst, b, h) do { _Pragma("unroll") for (int n = 0; n < 2; ++n) { const bf16x8 f0_ = *(const PG8_LAS bf16x8*)(lds + PG8_SB(b, h) + boff + n * 2048), f1_ = *(const PG8_LAS bf16x8*)(lds + PG8_SB(b, h) + boff + n * 2048 + 1024); dst[n].set(f0_, f1_); } } while (0)
; #define PG8_WAIT_V(n) asm volatile("s_waitcnt vmcnt(" #n ")" ::: "memory")
; #define PG8_WAIT_L(n) asm volatile("s_waitcnt lgkmcnt(" #n ")" ::: "memory")
; #define PG8_BAR __builtin_amdgcn_s_barrier()
; #define PG8_SCHED __builtin_amdgcn_sched_barrier(0)
; template <class Epi, class Sched, bool ALIGN_EPI = false, bool SP2 = false>
; __device__ __forceinline__ void gemm_phase(PG8_LAS unsigned char* lds, const Gemm g, const Sched& S, const Epi& E) {
;     ...
;             PG8_LDB(B0, 0, 0); PG8_LDB(B1, 0, 1); PG8_SCHED; PG8_LDA(At, 0, 0); PG8_STAGE(PG8_SA(1, 1), a1 + hstep, voffA);
;             PG8_WAIT_V(8); PG8_WAIT_L(0); PG8_BAR; PG8_MMA(0, 0, At, B0); PG8_MMA(0, 1, At, B1); PG8_BAR; PG8_SCHED;
;             PG8_LDA(At, 0, 1); PG8_STAGE(PG8_SB(0, 0), b2, voffB); PG8_STAGE(PG8_SB(0, 1), b2 + hstepB, voffB); PG8_STAGE(PG8_SA(0, 0), a2, voffA);
;             PG8_WAIT_V(8); PG8_WAIT_L(0); PG8_BAR; PG8_MMA(1, 0, At, B0); PG8_MMA(1, 1, At, B1); PG8_BAR; PG8_SCHED;
.LBB0_204:
	ds_read_b128 v[18:21], v203
	ds_read_b128 v[22:25], v203 offset:1024
	ds_read_b128 v[26:29], v203 offset:2048
	ds_read_b128 v[30:33], v203 offset:3072
	ds_read_b128 v[2:5], v204
	ds_read_b128 v[6:9], v204 offset:1024
	ds_read_b128 v[10:13], v204 offset:2048
	ds_read_b128 v[14:17], v204 offset:3072
	s_add_i32 s53, s48, 2
	s_add_u32 s0, s2, 0x80
	s_addc_u32 s1, s3, 0
	s_cmp_eq_u32 s71, s48
	s_cselect_b32 s48, s44, s0
	s_cselect_b32 s49, s45, s1
	s_cselect_b32 s51, s47, s52
	s_cselect_b32 s50, s46, s20
	v_lshl_add_u64 v[190:191], s[2:3], 0, v[174:175]
	s_add_i32 m0, s58, 0xc000
	ds_read_b128 v[182:185], v205
	ds_read_b128 v[186:189], v205 offset:1024
	ds_read_b128 v[212:215], v205 offset:2048
	ds_read_b128 v[216:219], v205 offset:3072
	ds_read_b128 v[220:223], v205 offset:4096
	ds_read_b128 v[224:227], v205 offset:5120
	ds_read_b128 v[228:231], v205 offset:6144
	ds_read_b128 v[232:235], v205 offset:7168
	global_load_lds_dwordx4 v[190:191], off
	v_lshl_add_u64 v[190:191], s[2:3], 0, v[176:177]
	s_add_i32 m0, s58, 0xe000
	s_nop 0
	global_load_lds_dwordx4 v[190:191], off
	s_waitcnt vmcnt(8)
	s_waitcnt lgkmcnt(0)
	s_barrier
	s_setprio 1
	s_waitcnt lgkmcnt(0)
	v_mfma_scale_f32_16x16x128_f8f6f4 v[158:161], v[18:25], v[182:189], v[158:161], v206, v207 op_sel_hi:[0,0,0]
	v_mfma_scale_f32_16x16x128_f8f6f4 v[154:157], v[26:33], v[182:189], v[154:157], v206, v207 op_sel_hi:[0,0,0]
	v_mfma_scale_f32_16x16x128_f8f6f4 v[142:145], v[18:25], v[212:219], v[142:145], v206, v207 op_sel_hi:[0,0,0]
	v_mfma_scale_f32_16x16x128_f8f6f4 v[138:141], v[26:33], v[212:219], v[138:141], v206, v207 op_sel_hi:[0,0,0]
	v_mfma_scale_f32_16x16x128_f8f6f4 v[126:129], v[18:25], v[220:227], v[126:129], v206, v207 op_sel_hi:[0,0,0]
	v_mfma_scale_f32_16x16x128_f8f6f4 v[122:125], v[26:33], v[220:227], v[122:125], v206, v207 op_sel_hi:[0,0,0]
	v_mfma_scale_f32_16x16x128_f8f6f4 v[110:113], v[18:25], v[228:235], v[110:113], v206, v207 op_sel_hi:[0,0,0]
	v_mfma_scale_f32_16x16x128_f8f6f4 v[106:109], v[26:33], v[228:235], v[106:109], v206, v207 op_sel_hi:[0,0,0]
	s_setprio 0
	s_setprio 1
	v_mfma_scale_f32_16x16x128_f8f6f4 v[150:153], v[2:9], v[182:189], v[150:153], v206, v207 op_sel_hi:[0,0,0]
	v_mfma_scale_f32_16x16x128_f8f6f4 v[146:149], v[10:17], v[182:189], v[146:149], v206, v207 op_sel_hi:[0,0,0]
	v_mfma_scale_f32_16x16x128_f8f6f4 v[134:137], v[2:9], v[212:219], v[134:137], v206, v207 op_sel_hi:[0,0,0]
	v_mfma_scale_f32_16x16x128_f8f6f4 v[130:133], v[10:17], v[212:219], v[130:133], v206, v207 op_sel_hi:[0,0,0]
	v_mfma_scale_f32_16x16x128_f8f6f4 v[118:121], v[2:9], v[220:227], v[118:121], v206, v207 op_sel_hi:[0,0,0]
	v_mfma_scale_f32_16x16x128_f8f6f4 v[114:117], v[10:17], v[220:227], v[114:117], v206, v207 op_sel_hi:[0,0,0]
	v_mfma_scale_f32_16x16x128_f8f6f4 v[102:105], v[2:9], v[228:235], v[102:105], v206, v207 op_sel_hi:[0,0,0]
	v_mfma_scale_f32_16x16x128_f8f6f4 v[98:101], v[10:17], v[228:235], v[98:101], v206, v207 op_sel_hi:[0,0,0]
	s_setprio 0
	s_barrier
	s_add_i32 s0, s76, s57
	v_lshl_add_u64 v[182:183], s[50:51], 0, v[164:165]
	s_mov_b32 m0, s0
	ds_read_b128 v[212:215], v205 offset:16384
	ds_read_b128 v[216:219], v205 offset:17408
	ds_read_b128 v[220:223], v205 offset:18432
	ds_read_b128 v[224:227], v205 offset:19456
	ds_read_b128 v[228:231], v205 offset:20480
	ds_read_b128 v[232:235], v205 offset:21504
	ds_read_b128 v[236:239], v205 offset:22528
	ds_read_b128 v[240:243], v205 offset:23552
	global_load_lds_dwordx4 v[182:183], off
	s_add_i32 m0, s0, 0x2000
	v_lshl_add_u64 v[184:185], s[50:51], 0, v[168:169]
	s_add_u32 s50, s50, s16
	s_addc_u32 s51, s51, s17
	s_add_i32 s0, s77, s57
	global_load_lds_dwordx4 v[184:185], off
	v_lshl_add_u64 v[186:187], s[50:51], 0, v[164:165]
	s_mov_b32 m0, s0
	v_lshl_add_u64 v[188:189], s[50:51], 0, v[168:169]
	global_load_lds_dwordx4 v[186:187], off
	s_add_i32 m0, s0, 0x2000
	v_lshl_add_u64 v[190:191], s[48:49], 0, v[162:163]
	global_load_lds_dwordx4 v[188:189], off
	v_lshl_add_u64 v[192:193], s[48:49], 0, v[166:167]
	s_waitcnt vmcnt(6)
	s_waitcnt lgkmcnt(0)
	s_barrier
	s_setprio 1
	s_waitcnt lgkmcnt(0)
	v_mfma_scale_f32_16x16x128_f8f6f4 v[94:97], v[18:25], v[212:219], v[94:97], v206, v207 op_sel_hi:[0,0,0]
	v_mfma_scale_f32_16x16x128_f8f6f4 v[90:93], v[26:33], v[212:219], v[90:93], v206, v207 op_sel_hi:[0,0,0]
	v_mfma_scale_f32_16x16x128_f8f6f4 v[78:81], v[18:25], v[220:227], v[78:81], v206, v207 op_sel_hi:[0,0,0]
	v_mfma_scale_f32_16x16x128_f8f6f4 v[74:77], v[26:33], v[220:227], v[74:77], v206, v207 op_sel_hi:[0,0,0]
	v_mfma_scale_f32_16x16x128_f8f6f4 v[62:65], v[18:25], v[228:235], v[62:65], v206, v207 op_sel_hi:[0,0,0]
	v_mfma_scale_f32_16x16x128_f8f6f4 v[58:61], v[26:33], v[228:235], v[58:61], v206, v207 op_sel_hi:[0,0,0]
	v_mfma_scale_f32_16x16x128_f8f6f4 v[46:49], v[18:25], v[236:243], v[46:49], v206, v207 op_sel_hi:[0,0,0]
	v_mfma_scale_f32_16x16x128_f8f6f4 v[42:45], v[26:33], v[236:243], v[42:45], v206, v207 op_sel_hi:[0,0,0]
	s_setprio 0
	s_setprio 1
	v_mfma_scale_f32_16x16x128_f8f6f4 v[86:89], v[2:9], v[212:219], v[86:89], v206, v207 op_sel_hi:[0,0,0]
	v_mfma_scale_f32_16x16x128_f8f6f4 v[82:85], v[10:17], v[212:219], v[82:85], v206, v207 op_sel_hi:[0,0,0]
	v_mfma_scale_f32_16x16x128_f8f6f4 v[70:73], v[2:9], v[220:227], v[70:73], v206, v207 op_sel_hi:[0,0,0]
	v_mfma_scale_f32_16x16x128_f8f6f4 v[66:69], v[10:17], v[220:227], v[66:69], v206, v207 op_sel_hi:[0,0,0]
	v_mfma_scale_f32_16x16x128_f8f6f4 v[54:57], v[2:9], v[228:235], v[54:57], v206, v207 op_sel_hi:[0,0,0]
	v_mfma_scale_f32_16x16x128_f8f6f4 v[50:53], v[10:17], v[228:235], v[50:53], v206, v207 op_sel_hi:[0,0,0]
	v_mfma_scale_f32_16x16x128_f8f6f4 v[38:41], v[2:9], v[236:243], v[38:41], v206, v207 op_sel_hi:[0,0,0]
	v_mfma_scale_f32_16x16x128_f8f6f4 v[34:37], v[10:17], v[236:243], v[34:37], v206, v207 op_sel_hi:[0,0,0]
	s_setprio 0
	s_barrier
; #define PG8_STAGE(bufoff, gbase, voff) do { _Pragma("unroll") for (int _i = 0; _i < 2; ++_i) \
;         __builtin_amdgcn_global_load_lds((const unsigned*)((const char*)(gbase) + (voff)[_i]), (PG8_LAS unsigned*)(lds + (bufoff) + ldsw + _i * 8192), 16, 0, 0); } while (0)
; #define PG8_LDA(dst, b, h) do { _Pragma("unroll") for (int m = 0; m < 4; ++m) { const bf16x8 f0_ = *(const PG8_LAS bf16x8*)(lds + PG8_SA(b, h) + aoff + m * 2048), f1_ = *(const PG8_LAS bf16x8*)(lds + PG8_SA(b, h) + aoff + m * 2048 + 1024); dst[m].set(f0_, f1_); } } while (0)
; #define PG8_LDB(dst, b, h) do { _Pragma("unroll") for (int n = 0; n < 2; ++n) { const bf16x8 f0_ = *(const PG8_LAS bf16x8*)(lds + PG8_SB(b, h) + boff + n * 2048), f1_ = *(const PG8_LAS bf16x8*)(lds + PG8_SB(b, h) + boff + n * 2048 + 1024); dst[n].set(f0_, f1_); } } while (0)
; #define PG8_WAIT_V(n) asm volatile("s_waitcnt vmcnt(" #n ")" ::: "memory")
; #define PG8_WAIT_L(n) asm volatile("s_waitcnt lgkmcnt(" #n ")" ::: "memory")
; #define PG8_BAR __builtin_amdgcn_s_barrier()
; #define PG8_SCHED __builtin_amdgcn_sched_barrier(0)
; template <class Epi, class Sched, bool ALIGN_EPI = false, bool SP2 = false>
; __device__ __forceinline__ void gemm_phase(PG8_LAS unsigned char* lds, const Gemm g, const Sched& S, const Epi& E) {
;     ...
;             PG8_LDB(B0, 1, 0); PG8_LDB(B1, 1, 1); PG8_SCHED; PG8_LDA(At, 1, 0); PG8_STAGE(PG8_SA(0, 1), a2 + hstep, voffA);
;             PG8_WAIT_V(8); PG8_WAIT_L(0); PG8_BAR; PG8_MMA(0, 0, At, B0); PG8_MMA(0, 1, At, B1); PG8_BAR; PG8_SCHED;
;             PG8_LDA(At, 1, 1); PG8_STAGE(PG8_SB(1, 0), b3, voffB); PG8_STAGE(PG8_SB(1, 1), b3 + hstepB, voffB); PG8_STAGE(PG8_SA(1, 0), a3, voffA);
;             PG8_WAIT_V(8); PG8_WAIT_L(0); PG8_BAR; PG8_MMA(1, 0, At, B0); PG8_MMA(1, 1, At, B1); PG8_BAR; PG8_SCHED;
	s_add_i32 s0, 0, 0x18000
	s_add_i32 s1, 0, 0x1c000
	v_add_u32_e32 v14, s0, v194
	v_add_u32_e32 v30, s1, v194
	ds_read_b128 v[2:5], v14
	ds_read_b128 v[6:9], v14 offset:1024
	ds_read_b128 v[10:13], v14 offset:2048
	ds_read_b128 v[14:17], v14 offset:3072
	ds_read_b128 v[18:21], v30
	ds_read_b128 v[22:25], v30 offset:1024
	ds_read_b128 v[26:29], v30 offset:2048
	ds_read_b128 v[30:33], v30 offset:3072
	s_add_u32 s48, s48, s14
	s_addc_u32 s49, s49, s15
	s_mov_b32 m0, s61
	v_lshl_add_u64 v[244:245], s[48:49], 0, v[162:163]
	ds_read_b128 v[212:215], v205 offset:32768
	ds_read_b128 v[216:219], v205 offset:33792
	ds_read_b128 v[220:223], v205 offset:34816
	ds_read_b128 v[224:227], v205 offset:35840
	ds_read_b128 v[228:231], v205 offset:36864
	ds_read_b128 v[232:235], v205 offset:37888
	ds_read_b128 v[236:239], v205 offset:38912
	ds_read_b128 v[240:243], v205 offset:39936
	global_load_lds_dwordx4 v[244:245], off
	v_lshl_add_u64 v[244:245], s[48:49], 0, v[166:167]
	s_mov_b32 m0, s63
	s_nop 0
	global_load_lds_dwordx4 v[244:245], off
	s_mov_b32 m0, s58
	s_nop 0
	global_load_lds_dwordx4 v[190:191], off
	s_mov_b32 m0, s59
	s_nop 0
	global_load_lds_dwordx4 v[192:193], off
	s_waitcnt vmcnt(8)
	s_waitcnt lgkmcnt(0)
	s_barrier
	s_setprio 1
	s_waitcnt lgkmcnt(0)
	v_mfma_scale_f32_16x16x128_f8f6f4 v[158:161], v[2:9], v[212:219], v[158:161], v206, v207 op_sel_hi:[0,0,0]
	v_mfma_scale_f32_16x16x128_f8f6f4 v[154:157], v[10:17], v[212:219], v[154:157], v206, v207 op_sel_hi:[0,0,0]
	v_mfma_scale_f32_16x16x128_f8f6f4 v[142:145], v[2:9], v[220:227], v[142:145], v206, v207 op_sel_hi:[0,0,0]
	v_mfma_scale_f32_16x16x128_f8f6f4 v[138:141], v[10:17], v[220:227], v[138:141], v206, v207 op_sel_hi:[0,0,0]
	v_mfma_scale_f32_16x16x128_f8f6f4 v[126:129], v[2:9], v[228:235], v[126:129], v206, v207 op_sel_hi:[0,0,0]
	v_mfma_scale_f32_16x16x128_f8f6f4 v[122:125], v[10:17], v[228:235], v[122:125], v206, v207 op_sel_hi:[0,0,0]
	v_mfma_scale_f32_16x16x128_f8f6f4 v[110:113], v[2:9], v[236:243], v[110:113], v206, v207 op_sel_hi:[0,0,0]
	v_mfma_scale_f32_16x16x128_f8f6f4 v[106:109], v[10:17], v[236:243], v[106:109], v206, v207 op_sel_hi:[0,0,0]
	s_setprio 0
	s_setprio 1
	v_mfma_scale_f32_16x16x128_f8f6f4 v[150:153], v[18:25], v[212:219], v[150:153], v206, v207 op_sel_hi:[0,0,0]
	v_mfma_scale_f32_16x16x128_f8f6f4 v[146:149], v[26:33], v[212:219], v[146:149], v206, v207 op_sel_hi:[0,0,0]
	v_mfma_scale_f32_16x16x128_f8f6f4 v[134:137], v[18:25], v[220:227], v[134:137], v206, v207 op_sel_hi:[0,0,0]
	v_mfma_scale_f32_16x16x128_f8f6f4 v[130:133], v[26:33], v[220:227], v[130:133], v206, v207 op_sel_hi:[0,0,0]
	v_mfma_scale_f32_16x16x128_f8f6f4 v[118:121], v[18:25], v[228:235], v[118:121], v206, v207 op_sel_hi:[0,0,0]
	v_mfma_scale_f32_16x16x128_f8f6f4 v[114:117], v[26:33], v[228:235], v[114:117], v206, v207 op_sel_hi:[0,0,0]
	v_mfma_scale_f32_16x16x128_f8f6f4 v[102:105], v[18:25], v[236:243], v[102:105], v206, v207 op_sel_hi:[0,0,0]
	v_mfma_scale_f32_16x16x128_f8f6f4 v[98:101], v[26:33], v[236:243], v[98:101], v206, v207 op_sel_hi:[0,0,0]
	s_setprio 0
	s_barrier
	s_add_i32 s0, s0, s57
	v_lshl_add_u64 v[182:183], v[182:183], 0, s[36:37]
	s_mov_b32 m0, s0
	ds_read_b128 v[212:215], v205 offset:49152
	ds_read_b128 v[216:219], v205 offset:50176
	ds_read_b128 v[220:223], v205 offset:51200
	ds_read_b128 v[224:227], v205 offset:52224
	ds_read_b128 v[228:231], v205 offset:53248
	ds_read_b128 v[232:235], v205 offset:54272
	ds_read_b128 v[236:239], v205 offset:55296
	ds_read_b128 v[240:243], v205 offset:56320
	global_load_lds_dwordx4 v[182:183], off
	v_lshl_add_u64 v[182:183], v[184:185], 0, s[36:37]
	s_add_i32 m0, s0, 0x2000
	s_add_i32 s0, s1, s57
	global_load_lds_dwordx4 v[182:183], off
	v_lshl_add_u64 v[182:183], v[186:187], 0, s[36:37]
	s_mov_b32 m0, s0
	s_nop 0
	global_load_lds_dwordx4 v[182:183], off
	v_lshl_add_u64 v[182:183], v[188:189], 0, s[36:37]
	s_add_i32 m0, s0, 0x2000
	s_nop 0
	global_load_lds_dwordx4 v[182:183], off
	v_lshl_add_u64 v[182:183], v[190:191], 0, s[36:37]
	s_mov_b32 m0, s66
	s_nop 0
	global_load_lds_dwordx4 v[182:183], off
	v_lshl_add_u64 v[182:183], v[192:193], 0, s[36:37]
	s_mov_b32 m0, s67
	s_nop 0
	global_load_lds_dwordx4 v[182:183], off
	s_waitcnt vmcnt(6)
	s_waitcnt lgkmcnt(0)
	s_barrier
	s_setprio 1
	s_waitcnt lgkmcnt(0)
	v_mfma_scale_f32_16x16x128_f8f6f4 v[94:97], v[2:9], v[212:219], v[94:97], v206, v207 op_sel_hi:[0,0,0]
	v_mfma_scale_f32_16x16x128_f8f6f4 v[90:93], v[10:17], v[212:219], v[90:93], v206, v207 op_sel_hi:[0,0,0]
	v_mfma_scale_f32_16x16x128_f8f6f4 v[78:81], v[2:9], v[220:227], v[78:81], v206, v207 op_sel_hi:[0,0,0]
	v_mfma_scale_f32_16x16x128_f8f6f4 v[74:77], v[10:17], v[220:227], v[74:77], v206, v207 op_sel_hi:[0,0,0]
	v_mfma_scale_f32_16x16x128_f8f6f4 v[62:65], v[2:9], v[228:235], v[62:65], v206, v207 op_sel_hi:[0,0,0]
	v_mfma_scale_f32_16x16x128_f8f6f4 v[58:61], v[10:17], v[228:235], v[58:61], v206, v207 op_sel_hi:[0,0,0]
	v_mfma_scale_f32_16x16x128_f8f6f4 v[46:49], v[2:9], v[236:243], v[46:49], v206, v207 op_sel_hi:[0,0,0]
	v_mfma_scale_f32_16x16x128_f8f6f4 v[42:45], v[10:17], v[236:243], v[42:45], v206, v207 op_sel_hi:[0,0,0]
	s_setprio 0
	s_setprio 1
	v_mfma_scale_f32_16x16x128_f8f6f4 v[86:89], v[18:25], v[212:219], v[86:89], v206, v207 op_sel_hi:[0,0,0]
	v_mfma_scale_f32_16x16x128_f8f6f4 v[82:85], v[26:33], v[212:219], v[82:85], v206, v207 op_sel_hi:[0,0,0]
	v_mfma_scale_f32_16x16x128_f8f6f4 v[70:73], v[18:25], v[220:227], v[70:73], v206, v207 op_sel_hi:[0,0,0]
	v_mfma_scale_f32_16x16x128_f8f6f4 v[66:69], v[26:33], v[220:227], v[66:69], v206, v207 op_sel_hi:[0,0,0]
	v_mfma_scale_f32_16x16x128_f8f6f4 v[54:57], v[18:25], v[228:235], v[54:57], v206, v207 op_sel_hi:[0,0,0]
	v_mfma_scale_f32_16x16x128_f8f6f4 v[50:53], v[26:33], v[228:235], v[50:53], v206, v207 op_sel_hi:[0,0,0]
	v_mfma_scale_f32_16x16x128_f8f6f4 v[38:41], v[18:25], v[236:243], v[38:41], v206, v207 op_sel_hi:[0,0,0]
	v_mfma_scale_f32_16x16x128_f8f6f4 v[34:37], v[26:33], v[236:243], v[34:37], v206, v207 op_sel_hi:[0,0,0]
	s_setprio 0
	s_barrier
	s_add_u32 s2, s2, 0x100
	s_addc_u32 s3, s3, 0
	s_add_u32 s20, s20, 0x100
	s_addc_u32 s52, s52, 0
	s_cmp_ge_i32 s53, s69
	s_mov_b32 s48, s53
	s_cbranch_scc0 .LBB0_204

; #define PG8_STAGE(bufoff, gbase, voff) do { _Pragma("unroll") for (int _i = 0; _i < 2; ++_i) \
;         __builtin_amdgcn_global_load_lds((const unsigned*)((const char*)(gbase) + (voff)[_i]), (PG8_LAS unsigned*)(lds + (bufoff) + ldsw + _i * 8192), 16, 0, 0); } while (0)
; #define PG8_LDA(dst, b, h) do { _Pragma("unroll") for (int m = 0; m < 4; ++m) { const bf16x8 f0_ = *(const PG8_LAS bf16x8*)(lds + PG8_SA(b, h) + aoff + m * 2048), f1_ = *(const PG8_LAS bf16x8*)(lds + PG8_SA(b, h) + aoff + m * 2048 + 1024); dst[m].set(f0_, f1_); } } while (0)
; #define PG8_LDB(dst, b, h) do { _Pragma("unroll") for (int n = 0; n < 2; ++n) { const bf16x8 f0_ = *(const PG8_LAS bf16x8*)(lds + PG8_SB(b, h) + boff + n * 2048), f1_ = *(const PG8_LAS bf16x8*)(lds + PG8_SB(b, h) + boff + n * 2048 + 1024); dst[n].set(f0_, f1_); } } while (0)
; #define PG8_WAIT_V(n) asm volatile("s_waitcnt vmcnt(" #n ")" ::: "memory")
; #define PG8_WAIT_L(n) asm volatile("s_waitcnt lgkmcnt(" #n ")" ::: "memory")
; #define PG8_BAR __builtin_amdgcn_s_barrier()
; #define PG8_SCHED __builtin_amdgcn_sched_barrier(0)
; template <class Epi, class Sched, bool ALIGN_EPI = false, bool SP2 = false>
; __device__ __forceinline__ void gemm_phase(PG8_LAS unsigned char* lds, const Gemm g, const Sched& S, const Epi& E) {
;     ...
;             PG8_LDB(B0, 0, 0); PG8_LDB(B1, 0, 1); PG8_SCHED; PG8_LDA(At, 0, 0); PG8_STAGE(PG8_SA(1, 1), a1 + hstep, voffA);
;             PG8_WAIT_V(8); PG8_WAIT_L(0); PG8_BAR; PG8_MMA(0, 0, At, B0); PG8_MMA(0, 1, At, B1); PG8_BAR; PG8_SCHED;
;             PG8_LDA(At, 0, 1); PG8_STAGE(PG8_SB(0, 0), b2, voffB); PG8_STAGE(PG8_SB(0, 1), b2 + hstepB, voffB); PG8_STAGE(PG8_SA(0, 0), a2, voffA);
;             PG8_WAIT_V(8); PG8_WAIT_L(0); PG8_BAR; PG8_MMA(1, 0, At, B0); PG8_MMA(1, 1, At, B1); PG8_BAR; PG8_SCHED;
.LBB0_984:
	s_add_i32 s75, s42, 2
	v_add_u32_e32 v186, s59, v173
	v_add_u32_e32 v202, s61, v173
	s_add_u32 s0, s38, s40
	ds_read_b128 v[168:171], v186
	ds_read_b128 v[178:181], v186 offset:1024
	ds_read_b128 v[182:185], v186 offset:2048
	ds_read_b128 v[186:189], v186 offset:3072
	ds_read_b128 v[190:193], v202
	ds_read_b128 v[194:197], v202 offset:1024
	ds_read_b128 v[198:201], v202 offset:2048
	ds_read_b128 v[202:205], v202 offset:3072
	s_addc_u32 s1, s39, s41
	s_add_u32 s0, s0, 0x100
	s_addc_u32 s1, s1, 0
	s_add_u32 s33, s73, s40
	s_addc_u32 s76, s74, s41
	s_cmp_eq_u32 s57, s42
	s_cselect_b32 s43, s3, s1
	s_cselect_b32 s42, s2, s0
	s_cselect_b32 s1, s37, s76
	s_cselect_b32 s0, s36, s33
	v_lshl_add_u64 v[240:241], v[164:165], 0, s[40:41]
	s_add_i32 m0, s47, 0xc000
	ds_read_b128 v[206:209], v176
	ds_read_b128 v[212:215], v176 offset:1024
	ds_read_b128 v[216:219], v176 offset:2048
	ds_read_b128 v[220:223], v176 offset:3072
	ds_read_b128 v[224:227], v176 offset:4096
	ds_read_b128 v[228:231], v176 offset:5120
	ds_read_b128 v[232:235], v176 offset:6144
	ds_read_b128 v[236:239], v176 offset:7168
	global_load_lds_dwordx4 v[240:241], off
	v_lshl_add_u64 v[240:241], v[166:167], 0, s[40:41]
	s_add_i32 m0, s47, 0xe000
	s_nop 0
	global_load_lds_dwordx4 v[240:241], off
	s_waitcnt vmcnt(8)
	s_waitcnt lgkmcnt(0)
	s_barrier
	s_setprio 1
	s_waitcnt lgkmcnt(0)
	v_mfma_f32_16x16x32_bf16 v[126:129], v[168:171], v[206:209], v[126:129]
	v_mfma_f32_16x16x32_bf16 v[122:125], v[182:185], v[206:209], v[122:125]
	v_mfma_f32_16x16x32_bf16 v[110:113], v[168:171], v[216:219], v[110:113]
	v_mfma_f32_16x16x32_bf16 v[106:109], v[182:185], v[216:219], v[106:109]
	v_mfma_f32_16x16x32_bf16 v[94:97], v[168:171], v[224:227], v[94:97]
	v_mfma_f32_16x16x32_bf16 v[90:93], v[182:185], v[224:227], v[90:93]
	v_mfma_f32_16x16x32_bf16 v[78:81], v[168:171], v[232:235], v[78:81]
	v_mfma_f32_16x16x32_bf16 v[74:77], v[182:185], v[232:235], v[74:77]
	v_mfma_f32_16x16x32_bf16 v[126:129], v[178:181], v[212:215], v[126:129]
	v_mfma_f32_16x16x32_bf16 v[122:125], v[186:189], v[212:215], v[122:125]
	v_mfma_f32_16x16x32_bf16 v[110:113], v[178:181], v[220:223], v[110:113]
	v_mfma_f32_16x16x32_bf16 v[106:109], v[186:189], v[220:223], v[106:109]
	v_mfma_f32_16x16x32_bf16 v[94:97], v[178:181], v[228:231], v[94:97]
	v_mfma_f32_16x16x32_bf16 v[90:93], v[186:189], v[228:231], v[90:93]
	v_mfma_f32_16x16x32_bf16 v[78:81], v[178:181], v[236:239], v[78:81]
	v_mfma_f32_16x16x32_bf16 v[74:77], v[186:189], v[236:239], v[74:77]
	s_setprio 0
	s_setprio 1
	v_mfma_f32_16x16x32_bf16 v[118:121], v[190:193], v[206:209], v[118:121]
	v_mfma_f32_16x16x32_bf16 v[114:117], v[198:201], v[206:209], v[114:117]
	v_mfma_f32_16x16x32_bf16 v[102:105], v[190:193], v[216:219], v[102:105]
	v_mfma_f32_16x16x32_bf16 v[98:101], v[198:201], v[216:219], v[98:101]
	v_mfma_f32_16x16x32_bf16 v[86:89], v[190:193], v[224:227], v[86:89]
	v_mfma_f32_16x16x32_bf16 v[82:85], v[198:201], v[224:227], v[82:85]
	v_mfma_f32_16x16x32_bf16 v[70:73], v[190:193], v[232:235], v[70:73]
	v_mfma_f32_16x16x32_bf16 v[66:69], v[198:201], v[232:235], v[66:69]
	v_mfma_f32_16x16x32_bf16 v[118:121], v[194:197], v[212:215], v[118:121]
	v_mfma_f32_16x16x32_bf16 v[114:117], v[202:205], v[212:215], v[114:117]
	v_mfma_f32_16x16x32_bf16 v[102:105], v[194:197], v[220:223], v[102:105]
	v_mfma_f32_16x16x32_bf16 v[98:101], v[202:205], v[220:223], v[98:101]
	v_mfma_f32_16x16x32_bf16 v[86:89], v[194:197], v[228:231], v[86:89]
	v_mfma_f32_16x16x32_bf16 v[82:85], v[202:205], v[228:231], v[82:85]
	v_mfma_f32_16x16x32_bf16 v[70:73], v[194:197], v[236:239], v[70:73]
	v_mfma_f32_16x16x32_bf16 v[66:69], v[202:205], v[236:239], v[66:69]
	s_setprio 0
	s_barrier
	s_add_i32 s33, s59, s46
	v_lshl_add_u64 v[240:241], s[0:1], 0, v[132:133]
	s_mov_b32 m0, s33
	ds_read_b128 v[206:209], v176 offset:16384
	ds_read_b128 v[212:215], v176 offset:17408
	ds_read_b128 v[216:219], v176 offset:18432
	ds_read_b128 v[220:223], v176 offset:19456
	ds_read_b128 v[224:227], v176 offset:20480
	ds_read_b128 v[228:231], v176 offset:21504
	ds_read_b128 v[232:235], v176 offset:22528
	ds_read_b128 v[236:239], v176 offset:23552
	global_load_lds_dwordx4 v[240:241], off
	s_add_i32 m0, s33, 0x2000
	v_lshl_add_u64 v[242:243], s[0:1], 0, v[136:137]
	s_add_u32 s0, s0, s14
	s_addc_u32 s1, s1, s15
	s_add_i32 s33, s61, s46
	global_load_lds_dwordx4 v[242:243], off
	v_lshl_add_u64 v[244:245], s[0:1], 0, v[132:133]
	s_mov_b32 m0, s33
	v_lshl_add_u64 v[246:247], s[0:1], 0, v[136:137]
	global_load_lds_dwordx4 v[244:245], off
	s_add_i32 m0, s33, 0x2000
	v_lshl_add_u64 v[248:249], s[42:43], 0, v[130:131]
	global_load_lds_dwordx4 v[246:247], off
	v_lshl_add_u64 v[250:251], s[42:43], 0, v[134:135]
	s_waitcnt vmcnt(6)
	s_waitcnt lgkmcnt(0)
	s_barrier
; #define PG8_STAGE(bufoff, gbase, voff) do { _Pragma("unroll") for (int _i = 0; _i < 2; ++_i) \
;         __builtin_amdgcn_global_load_lds((const unsigned*)((const char*)(gbase) + (voff)[_i]), (PG8_LAS unsigned*)(lds + (bufoff) + ldsw + _i * 8192), 16, 0, 0); } while (0)
; #define PG8_LDA(dst, b, h) do { _Pragma("unroll") for (int m = 0; m < 4; ++m) { const bf16x8 f0_ = *(const PG8_LAS bf16x8*)(lds + PG8_SA(b, h) + aoff + m * 2048), f1_ = *(const PG8_LAS bf16x8*)(lds + PG8_SA(b, h) + aoff + m * 2048 + 1024); dst[m].set(f0_, f1_); } } while (0)
; #define PG8_LDB(dst, b, h) do { _Pragma("unroll") for (int n = 0; n < 2; ++n) { const bf16x8 f0_ = *(const PG8_LAS bf16x8*)(lds + PG8_SB(b, h) + boff + n * 2048), f1_ = *(const PG8_LAS bf16x8*)(lds + PG8_SB(b, h) + boff + n * 2048 + 1024); dst[n].set(f0_, f1_); } } while (0)
; #define PG8_WAIT_V(n) asm volatile("s_waitcnt vmcnt(" #n ")" ::: "memory")
; #define PG8_WAIT_L(n) asm volatile("s_waitcnt lgkmcnt(" #n ")" ::: "memory")
; #define PG8_BAR __builtin_amdgcn_s_barrier()
; #define PG8_SCHED __builtin_amdgcn_sched_barrier(0)
; template <class Epi, class Sched, bool ALIGN_EPI = false, bool SP2 = false>
; __device__ __forceinline__ void gemm_phase(PG8_LAS unsigned char* lds, const Gemm g, const Sched& S, const Epi& E) {
;     ...
;             PG8_WAIT_V(8); PG8_WAIT_L(0); PG8_BAR; PG8_MMA(1, 0, At, B0); PG8_MMA(1, 1, At, B1); PG8_BAR; PG8_SCHED;
;             PG8_LDB(B0, 1, 0); PG8_LDB(B1, 1, 1); PG8_SCHED; PG8_LDA(At, 1, 0); PG8_STAGE(PG8_SA(0, 1), a2 + hstep, voffA);
;             PG8_WAIT_V(8); PG8_WAIT_L(0); PG8_BAR; PG8_MMA(0, 0, At, B0); PG8_MMA(0, 1, At, B1); PG8_BAR; PG8_SCHED;
	s_setprio 1
	s_waitcnt lgkmcnt(0)
	v_mfma_f32_16x16x32_bf16 v[62:65], v[168:171], v[206:209], v[62:65]
	v_mfma_f32_16x16x32_bf16 v[58:61], v[182:185], v[206:209], v[58:61]
	v_mfma_f32_16x16x32_bf16 v[46:49], v[168:171], v[216:219], v[46:49]
	v_mfma_f32_16x16x32_bf16 v[42:45], v[182:185], v[216:219], v[42:45]
	v_mfma_f32_16x16x32_bf16 v[30:33], v[168:171], v[224:227], v[30:33]
	v_mfma_f32_16x16x32_bf16 v[26:29], v[182:185], v[224:227], v[26:29]
	v_mfma_f32_16x16x32_bf16 v[14:17], v[168:171], v[232:235], v[14:17]
	v_mfma_f32_16x16x32_bf16 v[10:13], v[182:185], v[232:235], v[10:13]
	v_mfma_f32_16x16x32_bf16 v[62:65], v[178:181], v[212:215], v[62:65]
	v_mfma_f32_16x16x32_bf16 v[58:61], v[186:189], v[212:215], v[58:61]
	v_mfma_f32_16x16x32_bf16 v[46:49], v[178:181], v[220:223], v[46:49]
	v_mfma_f32_16x16x32_bf16 v[42:45], v[186:189], v[220:223], v[42:45]
	v_mfma_f32_16x16x32_bf16 v[30:33], v[178:181], v[228:231], v[30:33]
	v_mfma_f32_16x16x32_bf16 v[26:29], v[186:189], v[228:231], v[26:29]
	v_mfma_f32_16x16x32_bf16 v[14:17], v[178:181], v[236:239], v[14:17]
	v_mfma_f32_16x16x32_bf16 v[10:13], v[186:189], v[236:239], v[10:13]
	s_setprio 0
	s_setprio 1
	v_mfma_f32_16x16x32_bf16 v[54:57], v[190:193], v[206:209], v[54:57]
	v_mfma_f32_16x16x32_bf16 v[50:53], v[198:201], v[206:209], v[50:53]
	v_mfma_f32_16x16x32_bf16 v[38:41], v[190:193], v[216:219], v[38:41]
	v_mfma_f32_16x16x32_bf16 v[34:37], v[198:201], v[216:219], v[34:37]
	v_mfma_f32_16x16x32_bf16 v[22:25], v[190:193], v[224:227], v[22:25]
	v_mfma_f32_16x16x32_bf16 v[18:21], v[198:201], v[224:227], v[18:21]
	v_mfma_f32_16x16x32_bf16 v[6:9], v[190:193], v[232:235], v[6:9]
	v_mfma_f32_16x16x32_bf16 v[2:5], v[198:201], v[232:235], v[2:5]
	v_mfma_f32_16x16x32_bf16 v[54:57], v[194:197], v[212:215], v[54:57]
	v_mfma_f32_16x16x32_bf16 v[50:53], v[202:205], v[212:215], v[50:53]
	v_mfma_f32_16x16x32_bf16 v[38:41], v[194:197], v[220:223], v[38:41]
	v_mfma_f32_16x16x32_bf16 v[34:37], v[202:205], v[220:223], v[34:37]
	v_mfma_f32_16x16x32_bf16 v[22:25], v[194:197], v[228:231], v[22:25]
	v_mfma_f32_16x16x32_bf16 v[18:21], v[202:205], v[228:231], v[18:21]
	v_mfma_f32_16x16x32_bf16 v[6:9], v[194:197], v[236:239], v[6:9]
	v_mfma_f32_16x16x32_bf16 v[2:5], v[202:205], v[236:239], v[2:5]
	s_setprio 0
	s_barrier
	s_add_i32 s33, 0, 0x18000
	s_add_i32 s76, 0, 0x1c000
	v_add_u32_e32 v186, s33, v173
	v_add_u32_e32 v202, s76, v173
	ds_read_b128 v[168:171], v186
	ds_read_b128 v[178:181], v186 offset:1024
	ds_read_b128 v[182:185], v186 offset:2048
	ds_read_b128 v[186:189], v186 offset:3072
	ds_read_b128 v[190:193], v202
	ds_read_b128 v[194:197], v202 offset:1024
	ds_read_b128 v[198:201], v202 offset:2048
	ds_read_b128 v[202:205], v202 offset:3072
	s_add_u32 s0, s42, s12
	s_addc_u32 s1, s43, s13
	s_mov_b32 m0, s49
	v_lshl_add_u64 v[252:253], s[0:1], 0, v[130:131]
	ds_read_b128 v[206:209], v176 offset:32768
	ds_read_b128 v[212:215], v176 offset:33792
	ds_read_b128 v[216:219], v176 offset:34816
	ds_read_b128 v[220:223], v176 offset:35840
	ds_read_b128 v[224:227], v176 offset:36864
	ds_read_b128 v[228:231], v176 offset:37888
	ds_read_b128 v[232:235], v176 offset:38912
	ds_read_b128 v[236:239], v176 offset:39936
	global_load_lds_dwordx4 v[252:253], off
	v_lshl_add_u64 v[252:253], s[0:1], 0, v[134:135]
	s_mov_b32 m0, s50
	s_nop 0
	global_load_lds_dwordx4 v[252:253], off
	s_mov_b32 m0, s47
	s_nop 0
	global_load_lds_dwordx4 v[248:249], off
	s_mov_b32 m0, s48
	s_nop 0
	global_load_lds_dwordx4 v[250:251], off
	s_waitcnt vmcnt(8)
	s_waitcnt lgkmcnt(0)
	s_barrier
	s_setprio 1
	s_waitcnt lgkmcnt(0)
	v_mfma_f32_16x16x32_bf16 v[126:129], v[168:171], v[206:209], v[126:129]
	v_mfma_f32_16x16x32_bf16 v[122:125], v[182:185], v[206:209], v[122:125]
	v_mfma_f32_16x16x32_bf16 v[110:113], v[168:171], v[216:219], v[110:113]
	v_mfma_f32_16x16x32_bf16 v[106:109], v[182:185], v[216:219], v[106:109]
	v_mfma_f32_16x16x32_bf16 v[94:97], v[168:171], v[224:227], v[94:97]
	v_mfma_f32_16x16x32_bf16 v[90:93], v[182:185], v[224:227], v[90:93]
	v_mfma_f32_16x16x32_bf16 v[78:81], v[168:171], v[232:235], v[78:81]
	v_mfma_f32_16x16x32_bf16 v[74:77], v[182:185], v[232:235], v[74:77]
	v_mfma_f32_16x16x32_bf16 v[126:129], v[178:181], v[212:215], v[126:129]
	v_mfma_f32_16x16x32_bf16 v[122:125], v[186:189], v[212:215], v[122:125]
	v_mfma_f32_16x16x32_bf16 v[110:113], v[178:181], v[220:223], v[110:113]
	v_mfma_f32_16x16x32_bf16 v[106:109], v[186:189], v[220:223], v[106:109]
	v_mfma_f32_16x16x32_bf16 v[94:97], v[178:181], v[228:231], v[94:97]
	v_mfma_f32_16x16x32_bf16 v[90:93], v[186:189], v[228:231], v[90:93]
	v_mfma_f32_16x16x32_bf16 v[78:81], v[178:181], v[236:239], v[78:81]
	v_mfma_f32_16x16x32_bf16 v[74:77], v[186:189], v[236:239], v[74:77]
	s_setprio 0
	s_setprio 1
	v_mfma_f32_16x16x32_bf16 v[118:121], v[190:193], v[206:209], v[118:121]
	v_mfma_f32_16x16x32_bf16 v[114:117], v[198:201], v[206:209], v[114:117]
	v_mfma_f32_16x16x32_bf16 v[102:105], v[190:193], v[216:219], v[102:105]
	v_mfma_f32_16x16x32_bf16 v[98:101], v[198:201], v[216:219], v[98:101]
	v_mfma_f32_16x16x32_bf16 v[86:89], v[190:193], v[224:227], v[86:89]
	v_mfma_f32_16x16x32_bf16 v[82:85], v[198:201], v[224:227], v[82:85]
	v_mfma_f32_16x16x32_bf16 v[70:73], v[190:193], v[232:235], v[70:73]
	v_mfma_f32_16x16x32_bf16 v[66:69], v[198:201], v[232:235], v[66:69]
	v_mfma_f32_16x16x32_bf16 v[118:121], v[194:197], v[212:215], v[118:121]
	v_mfma_f32_16x16x32_bf16 v[114:117], v[202:205], v[212:215], v[114:117]
	v_mfma_f32_16x16x32_bf16 v[102:105], v[194:197], v[220:223], v[102:105]
	v_mfma_f32_16x16x32_bf16 v[98:101], v[202:205], v[220:223], v[98:101]
	v_mfma_f32_16x16x32_bf16 v[86:89], v[194:197], v[228:231], v[86:89]
	v_mfma_f32_16x16x32_bf16 v[82:85], v[202:205], v[228:231], v[82:85]
	v_mfma_f32_16x16x32_bf16 v[70:73], v[194:197], v[236:239], v[70:73]
	v_mfma_f32_16x16x32_bf16 v[66:69], v[202:205], v[236:239], v[66:69]
	s_setprio 0
	s_barrier
; #define PG8_STAGE(bufoff, gbase, voff) do { _Pragma("unroll") for (int _i = 0; _i < 2; ++_i) \
;         __builtin_amdgcn_global_load_lds((const unsigned*)((const char*)(gbase) + (voff)[_i]), (PG8_LAS unsigned*)(lds + (bufoff) + ldsw + _i * 8192), 16, 0, 0); } while (0)
; #define PG8_LDA(dst, b, h) do { _Pragma("unroll") for (int m = 0; m < 4; ++m) { const bf16x8 f0_ = *(const PG8_LAS bf16x8*)(lds + PG8_SA(b, h) + aoff + m * 2048), f1_ = *(const PG8_LAS bf16x8*)(lds + PG8_SA(b, h) + aoff + m * 2048 + 1024); dst[m].set(f0_, f1_); } } while (0)
; #define PG8_WAIT_V(n) asm volatile("s_waitcnt vmcnt(" #n ")" ::: "memory")
; #define PG8_WAIT_L(n) asm volatile("s_waitcnt lgkmcnt(" #n ")" ::: "memory")
; #define PG8_BAR __builtin_amdgcn_s_barrier()
; #define PG8_SCHED __builtin_amdgcn_sched_barrier(0)
; template <class Epi, class Sched, bool ALIGN_EPI = false, bool SP2 = false>
; __device__ __forceinline__ void gemm_phase(PG8_LAS unsigned char* lds, const Gemm g, const Sched& S, const Epi& E) {
;     ...
;         for (int t = 0; t < nt; t += 2) {
;             if constexpr (Epi::MIDK) { if (t == (nt >> 1)) E.mid(acc, cur, wr, wc, fr, fq); }
;             const bool last = (t == nt - 2);
;             const char* a1 = cA + (size_t)(t + 1) * kstep;
;             const char* a2 = last ? nA : cA + (size_t)(t + 2) * kstep; const char* b2 = last ? nB : cB + (size_t)(t + 2) * kstep;
;             const char* a3 = a2 + kstep; const char* b3 = b2 + kstep;
;     ...
;             PG8_LDA(At, 1, 1); PG8_STAGE(PG8_SB(1, 0), b3, voffB); PG8_STAGE(PG8_SB(1, 1), b3 + hstepB, voffB); PG8_STAGE(PG8_SA(1, 0), a3, voffA);
;             PG8_WAIT_V(8); PG8_WAIT_L(0); PG8_BAR; PG8_MMA(1, 0, At, B0); PG8_MMA(1, 1, At, B1); PG8_BAR; PG8_SCHED;
	s_add_i32 s0, s33, s46
	v_lshl_add_u64 v[240:241], v[240:241], 0, s[26:27]
	s_mov_b32 m0, s0
	ds_read_b128 v[206:209], v176 offset:49152
	ds_read_b128 v[212:215], v176 offset:50176
	ds_read_b128 v[216:219], v176 offset:51200
	ds_read_b128 v[220:223], v176 offset:52224
	ds_read_b128 v[224:227], v176 offset:53248
	ds_read_b128 v[228:231], v176 offset:54272
	ds_read_b128 v[232:235], v176 offset:55296
	ds_read_b128 v[236:239], v176 offset:56320
	global_load_lds_dwordx4 v[240:241], off
	v_lshl_add_u64 v[240:241], v[242:243], 0, s[26:27]
	s_add_i32 m0, s0, 0x2000
	s_add_i32 s0, s76, s46
	global_load_lds_dwordx4 v[240:241], off
	v_lshl_add_u64 v[240:241], v[244:245], 0, s[26:27]
	s_mov_b32 m0, s0
	s_nop 0
	global_load_lds_dwordx4 v[240:241], off
	v_lshl_add_u64 v[240:241], v[246:247], 0, s[26:27]
	s_add_i32 m0, s0, 0x2000
	s_nop 0
	global_load_lds_dwordx4 v[240:241], off
	v_lshl_add_u64 v[240:241], v[248:249], 0, s[26:27]
	s_mov_b32 m0, s52
	s_nop 0
	global_load_lds_dwordx4 v[240:241], off
	v_lshl_add_u64 v[240:241], v[250:251], 0, s[26:27]
	s_mov_b32 m0, s53
	s_nop 0
	global_load_lds_dwordx4 v[240:241], off
	s_waitcnt vmcnt(6)
	s_waitcnt lgkmcnt(0)
	s_barrier
	s_setprio 1
	s_waitcnt lgkmcnt(0)
	v_mfma_f32_16x16x32_bf16 v[62:65], v[168:171], v[206:209], v[62:65]
	v_mfma_f32_16x16x32_bf16 v[58:61], v[182:185], v[206:209], v[58:61]
	v_mfma_f32_16x16x32_bf16 v[46:49], v[168:171], v[216:219], v[46:49]
	v_mfma_f32_16x16x32_bf16 v[42:45], v[182:185], v[216:219], v[42:45]
	v_mfma_f32_16x16x32_bf16 v[30:33], v[168:171], v[224:227], v[30:33]
	v_mfma_f32_16x16x32_bf16 v[26:29], v[182:185], v[224:227], v[26:29]
	v_mfma_f32_16x16x32_bf16 v[14:17], v[168:171], v[232:235], v[14:17]
	v_mfma_f32_16x16x32_bf16 v[10:13], v[182:185], v[232:235], v[10:13]
	v_mfma_f32_16x16x32_bf16 v[62:65], v[178:181], v[212:215], v[62:65]
	v_mfma_f32_16x16x32_bf16 v[58:61], v[186:189], v[212:215], v[58:61]
	v_mfma_f32_16x16x32_bf16 v[46:49], v[178:181], v[220:223], v[46:49]
	v_mfma_f32_16x16x32_bf16 v[42:45], v[186:189], v[220:223], v[42:45]
	v_mfma_f32_16x16x32_bf16 v[30:33], v[178:181], v[228:231], v[30:33]
	v_mfma_f32_16x16x32_bf16 v[26:29], v[186:189], v[228:231], v[26:29]
	v_mfma_f32_16x16x32_bf16 v[14:17], v[178:181], v[236:239], v[14:17]
	v_mfma_f32_16x16x32_bf16 v[10:13], v[186:189], v[236:239], v[10:13]
	s_setprio 0
	s_setprio 1
	v_mfma_f32_16x16x32_bf16 v[54:57], v[190:193], v[206:209], v[54:57]
	v_mfma_f32_16x16x32_bf16 v[50:53], v[198:201], v[206:209], v[50:53]
	v_mfma_f32_16x16x32_bf16 v[38:41], v[190:193], v[216:219], v[38:41]
	v_mfma_f32_16x16x32_bf16 v[34:37], v[198:201], v[216:219], v[34:37]
	v_mfma_f32_16x16x32_bf16 v[22:25], v[190:193], v[224:227], v[22:25]
	v_mfma_f32_16x16x32_bf16 v[18:21], v[198:201], v[224:227], v[18:21]
	v_mfma_f32_16x16x32_bf16 v[6:9], v[190:193], v[232:235], v[6:9]
	v_mfma_f32_16x16x32_bf16 v[2:5], v[198:201], v[232:235], v[2:5]
	v_mfma_f32_16x16x32_bf16 v[54:57], v[194:197], v[212:215], v[54:57]
	v_mfma_f32_16x16x32_bf16 v[50:53], v[202:205], v[212:215], v[50:53]
	v_mfma_f32_16x16x32_bf16 v[38:41], v[194:197], v[220:223], v[38:41]
	v_mfma_f32_16x16x32_bf16 v[34:37], v[202:205], v[220:223], v[34:37]
	v_mfma_f32_16x16x32_bf16 v[22:25], v[194:197], v[228:231], v[22:25]
	v_mfma_f32_16x16x32_bf16 v[18:21], v[202:205], v[228:231], v[18:21]
	v_mfma_f32_16x16x32_bf16 v[6:9], v[194:197], v[236:239], v[6:9]
	v_mfma_f32_16x16x32_bf16 v[2:5], v[202:205], v[236:239], v[2:5]
	s_setprio 0
	s_barrier
	s_add_u32 s40, s40, 0x100
	s_addc_u32 s41, s41, 0
	s_cmp_ge_i32 s75, s54
	s_cbranch_scc0 .LBB0_982

; #define PG8_STAGE(bufoff, gbase, voff) do { _Pragma("unroll") for (int _i = 0; _i < 2; ++_i) \
;         __builtin_amdgcn_global_load_lds((const unsigned*)((const char*)(gbase) + (voff)[_i]), (PG8_LAS unsigned*)(lds + (bufoff) + ldsw + _i * 8192), 16, 0, 0); } while (0)
; #define PG8_LDA(dst, b, h) do { _Pragma("unroll") for (int m = 0; m < 4; ++m) { const bf16x8 f0_ = *(const PG8_LAS bf16x8*)(lds + PG8_SA(b, h) + aoff + m * 2048), f1_ = *(const PG8_LAS bf16x8*)(lds + PG8_SA(b, h) + aoff + m * 2048 + 1024); dst[m].set(f0_, f1_); } } while (0)
; #define PG8_LDB(dst, b, h) do { _Pragma("unroll") for (int n = 0; n < 2; ++n) { const bf16x8 f0_ = *(const PG8_LAS bf16x8*)(lds + PG8_SB(b, h) + boff + n * 2048), f1_ = *(const PG8_LAS bf16x8*)(lds + PG8_SB(b, h) + boff + n * 2048 + 1024); dst[n].set(f0_, f1_); } } while (0)
; #define PG8_WAIT_V(n) asm volatile("s_waitcnt vmcnt(" #n ")" ::: "memory")
; #define PG8_WAIT_L(n) asm volatile("s_waitcnt lgkmcnt(" #n ")" ::: "memory")
; #define PG8_BAR __builtin_amdgcn_s_barrier()
; #define PG8_SCHED __builtin_amdgcn_sched_barrier(0)
; template <class Epi, class Sched, bool ALIGN_EPI = false, bool SP2 = false>
; __device__ __forceinline__ void gemm_phase(PG8_LAS unsigned char* lds, const Gemm g, const Sched& S, const Epi& E) {
;     ...
;             PG8_LDB(B0, 0, 0); PG8_LDB(B1, 0, 1); PG8_SCHED; PG8_LDA(At, 0, 0); PG8_STAGE(PG8_SA(1, 1), a1 + hstep, voffA);
;             PG8_WAIT_V(8); PG8_WAIT_L(0); PG8_BAR; PG8_MMA(0, 0, At, B0); PG8_MMA(0, 1, At, B1); PG8_BAR; PG8_SCHED;
;             PG8_LDA(At, 0, 1); PG8_STAGE(PG8_SB(0, 0), b2, voffB); PG8_STAGE(PG8_SB(0, 1), b2 + hstepB, voffB); PG8_STAGE(PG8_SA(0, 0), a2, voffA);
;             PG8_WAIT_V(8); PG8_WAIT_L(0); PG8_BAR; PG8_MMA(1, 0, At, B0); PG8_MMA(1, 1, At, B1); PG8_BAR; PG8_SCHED;
.LBB0_1070:
	ds_read_b128 v[130:133], v193
	ds_read_b128 v[134:137], v193 offset:1024
	ds_read_b128 v[138:141], v193 offset:2048
	ds_read_b128 v[142:145], v193 offset:3072
	ds_read_b128 v[146:149], v194
	ds_read_b128 v[150:153], v194 offset:1024
	ds_read_b128 v[154:157], v194 offset:2048
	ds_read_b128 v[158:161], v194 offset:3072
	s_add_i32 s95, s58, 2
	s_add_u32 s0, s56, 0x80
	s_addc_u32 s1, s57, 0
	s_cmp_eq_u32 s78, s58
	s_cselect_b32 s58, s2, s0
	s_cselect_b32 s59, s3, s1
	s_cselect_b32 s1, s55, s94
	s_cselect_b32 s0, s54, s93
	v_lshl_add_u64 v[224:225], s[56:57], 0, v[176:177]
	s_add_i32 m0, s67, 0xc000
	ds_read_b128 v[162:165], v195
	ds_read_b128 v[186:189], v195 offset:1024
	ds_read_b128 v[198:201], v195 offset:2048
	ds_read_b128 v[202:205], v195 offset:3072
	ds_read_b128 v[206:209], v195 offset:4096
	ds_read_b128 v[212:215], v195 offset:5120
	ds_read_b128 v[216:219], v195 offset:6144
	ds_read_b128 v[220:223], v195 offset:7168
	global_load_lds_dwordx4 v[224:225], off
	v_lshl_add_u64 v[224:225], s[56:57], 0, v[178:179]
	s_add_i32 m0, s67, 0xe000
	s_nop 0
	global_load_lds_dwordx4 v[224:225], off
	s_waitcnt vmcnt(8)
	s_waitcnt lgkmcnt(0)
	s_barrier
	s_setprio 1
	s_waitcnt lgkmcnt(0)
	v_mfma_f32_16x16x32_bf16 v[126:129], v[130:133], v[162:165], v[126:129]
	v_mfma_f32_16x16x32_bf16 v[122:125], v[138:141], v[162:165], v[122:125]
	v_mfma_f32_16x16x32_bf16 v[58:61], v[130:133], v[198:201], v[58:61]
	v_mfma_f32_16x16x32_bf16 v[62:65], v[138:141], v[198:201], v[62:65]
	v_mfma_f32_16x16x32_bf16 v[106:109], v[130:133], v[206:209], v[106:109]
	v_mfma_f32_16x16x32_bf16 v[110:113], v[138:141], v[206:209], v[110:113]
	v_mfma_f32_16x16x32_bf16 v[98:101], v[130:133], v[216:219], v[98:101]
	v_mfma_f32_16x16x32_bf16 v[102:105], v[138:141], v[216:219], v[102:105]
	v_mfma_f32_16x16x32_bf16 v[126:129], v[134:137], v[186:189], v[126:129]
	v_mfma_f32_16x16x32_bf16 v[122:125], v[142:145], v[186:189], v[122:125]
	v_mfma_f32_16x16x32_bf16 v[58:61], v[134:137], v[202:205], v[58:61]
	v_mfma_f32_16x16x32_bf16 v[62:65], v[142:145], v[202:205], v[62:65]
	v_mfma_f32_16x16x32_bf16 v[106:109], v[134:137], v[212:215], v[106:109]
	v_mfma_f32_16x16x32_bf16 v[110:113], v[142:145], v[212:215], v[110:113]
	v_mfma_f32_16x16x32_bf16 v[98:101], v[134:137], v[220:223], v[98:101]
	v_mfma_f32_16x16x32_bf16 v[102:105], v[142:145], v[220:223], v[102:105]
	s_setprio 0
	s_setprio 1
	v_mfma_f32_16x16x32_bf16 v[118:121], v[146:149], v[162:165], v[118:121]
	v_mfma_f32_16x16x32_bf16 v[114:117], v[154:157], v[162:165], v[114:117]
	v_mfma_f32_16x16x32_bf16 v[50:53], v[146:149], v[198:201], v[50:53]
	v_mfma_f32_16x16x32_bf16 v[54:57], v[154:157], v[198:201], v[54:57]
	v_mfma_f32_16x16x32_bf16 v[90:93], v[146:149], v[206:209], v[90:93]
	v_mfma_f32_16x16x32_bf16 v[94:97], v[154:157], v[206:209], v[94:97]
	v_mfma_f32_16x16x32_bf16 v[74:77], v[146:149], v[216:219], v[74:77]
	v_mfma_f32_16x16x32_bf16 v[78:81], v[154:157], v[216:219], v[78:81]
	v_mfma_f32_16x16x32_bf16 v[118:121], v[150:153], v[186:189], v[118:121]
	v_mfma_f32_16x16x32_bf16 v[114:117], v[158:161], v[186:189], v[114:117]
	v_mfma_f32_16x16x32_bf16 v[50:53], v[150:153], v[202:205], v[50:53]
	v_mfma_f32_16x16x32_bf16 v[54:57], v[158:161], v[202:205], v[54:57]
	v_mfma_f32_16x16x32_bf16 v[90:93], v[150:153], v[212:215], v[90:93]
	v_mfma_f32_16x16x32_bf16 v[94:97], v[158:161], v[212:215], v[94:97]
	v_mfma_f32_16x16x32_bf16 v[74:77], v[150:153], v[220:223], v[74:77]
	v_mfma_f32_16x16x32_bf16 v[78:81], v[158:161], v[220:223], v[78:81]
	s_setprio 0
	s_barrier
	s_add_i32 s33, s82, s66
	v_lshl_add_u64 v[224:225], s[0:1], 0, v[168:169]
	s_mov_b32 m0, s33
	ds_read_b128 v[162:165], v195 offset:16384
	ds_read_b128 v[186:189], v195 offset:17408
	ds_read_b128 v[198:201], v195 offset:18432
	ds_read_b128 v[202:205], v195 offset:19456
	ds_read_b128 v[206:209], v195 offset:20480
	ds_read_b128 v[212:215], v195 offset:21504
	ds_read_b128 v[216:219], v195 offset:22528
	ds_read_b128 v[220:223], v195 offset:23552
	global_load_lds_dwordx4 v[224:225], off
	s_add_i32 m0, s33, 0x2000
	v_lshl_add_u64 v[226:227], s[0:1], 0, v[172:173]
	s_add_u32 s0, s0, s16
	s_addc_u32 s1, s1, s17
	s_add_i32 s33, s83, s66
	global_load_lds_dwordx4 v[226:227], off
	v_lshl_add_u64 v[228:229], s[0:1], 0, v[168:169]
	s_mov_b32 m0, s33
	v_lshl_add_u64 v[230:231], s[0:1], 0, v[172:173]
	global_load_lds_dwordx4 v[228:229], off
	s_add_i32 m0, s33, 0x2000
	v_lshl_add_u64 v[232:233], s[58:59], 0, v[166:167]
	global_load_lds_dwordx4 v[230:231], off
	v_lshl_add_u64 v[234:235], s[58:59], 0, v[170:171]
	s_waitcnt vmcnt(6)
	s_waitcnt lgkmcnt(0)
	s_barrier
; #define PG8_STAGE(bufoff, gbase, voff) do { _Pragma("unroll") for (int _i = 0; _i < 2; ++_i) \
;         __builtin_amdgcn_global_load_lds((const unsigned*)((const char*)(gbase) + (voff)[_i]), (PG8_LAS unsigned*)(lds + (bufoff) + ldsw + _i * 8192), 16, 0, 0); } while (0)
; #define PG8_LDA(dst, b, h) do { _Pragma("unroll") for (int m = 0; m < 4; ++m) { const bf16x8 f0_ = *(const PG8_LAS bf16x8*)(lds + PG8_SA(b, h) + aoff + m * 2048), f1_ = *(const PG8_LAS bf16x8*)(lds + PG8_SA(b, h) + aoff + m * 2048 + 1024); dst[m].set(f0_, f1_); } } while (0)
; #define PG8_LDB(dst, b, h) do { _Pragma("unroll") for (int n = 0; n < 2; ++n) { const bf16x8 f0_ = *(const PG8_LAS bf16x8*)(lds + PG8_SB(b, h) + boff + n * 2048), f1_ = *(const PG8_LAS bf16x8*)(lds + PG8_SB(b, h) + boff + n * 2048 + 1024); dst[n].set(f0_, f1_); } } while (0)
; #define PG8_WAIT_V(n) asm volatile("s_waitcnt vmcnt(" #n ")" ::: "memory")
; #define PG8_WAIT_L(n) asm volatile("s_waitcnt lgkmcnt(" #n ")" ::: "memory")
; #define PG8_BAR __builtin_amdgcn_s_barrier()
; #define PG8_SCHED __builtin_amdgcn_sched_barrier(0)
; template <class Epi, class Sched, bool ALIGN_EPI = false, bool SP2 = false>
; __device__ __forceinline__ void gemm_phase(PG8_LAS unsigned char* lds, const Gemm g, const Sched& S, const Epi& E) {
;     ...
;             PG8_WAIT_V(8); PG8_WAIT_L(0); PG8_BAR; PG8_MMA(1, 0, At, B0); PG8_MMA(1, 1, At, B1); PG8_BAR; PG8_SCHED;
;             PG8_LDB(B0, 1, 0); PG8_LDB(B1, 1, 1); PG8_SCHED; PG8_LDA(At, 1, 0); PG8_STAGE(PG8_SA(0, 1), a2 + hstep, voffA);
;             PG8_WAIT_V(8); PG8_WAIT_L(0); PG8_BAR; PG8_MMA(0, 0, At, B0); PG8_MMA(0, 1, At, B1); PG8_BAR; PG8_SCHED;
	s_setprio 1
	s_waitcnt lgkmcnt(0)
	v_mfma_f32_16x16x32_bf16 v[82:85], v[130:133], v[162:165], v[82:85]
	v_mfma_f32_16x16x32_bf16 v[86:89], v[138:141], v[162:165], v[86:89]
	v_mfma_f32_16x16x32_bf16 v[46:49], v[130:133], v[198:201], v[46:49]
	v_mfma_f32_16x16x32_bf16 v[42:45], v[138:141], v[198:201], v[42:45]
	v_mfma_f32_16x16x32_bf16 v[30:33], v[130:133], v[206:209], v[30:33]
	v_mfma_f32_16x16x32_bf16 v[26:29], v[138:141], v[206:209], v[26:29]
	v_mfma_f32_16x16x32_bf16 v[14:17], v[130:133], v[216:219], v[14:17]
	v_mfma_f32_16x16x32_bf16 v[6:9], v[138:141], v[216:219], v[6:9]
	v_mfma_f32_16x16x32_bf16 v[82:85], v[134:137], v[186:189], v[82:85]
	v_mfma_f32_16x16x32_bf16 v[86:89], v[142:145], v[186:189], v[86:89]
	v_mfma_f32_16x16x32_bf16 v[46:49], v[134:137], v[202:205], v[46:49]
	v_mfma_f32_16x16x32_bf16 v[42:45], v[142:145], v[202:205], v[42:45]
	v_mfma_f32_16x16x32_bf16 v[30:33], v[134:137], v[212:215], v[30:33]
	v_mfma_f32_16x16x32_bf16 v[26:29], v[142:145], v[212:215], v[26:29]
	v_mfma_f32_16x16x32_bf16 v[14:17], v[134:137], v[220:223], v[14:17]
	v_mfma_f32_16x16x32_bf16 v[6:9], v[142:145], v[220:223], v[6:9]
	s_setprio 0
	s_setprio 1
	v_mfma_f32_16x16x32_bf16 v[66:69], v[146:149], v[162:165], v[66:69]
	v_mfma_f32_16x16x32_bf16 v[70:73], v[154:157], v[162:165], v[70:73]
	v_mfma_f32_16x16x32_bf16 v[38:41], v[146:149], v[198:201], v[38:41]
	v_mfma_f32_16x16x32_bf16 v[34:37], v[154:157], v[198:201], v[34:37]
	v_mfma_f32_16x16x32_bf16 v[22:25], v[146:149], v[206:209], v[22:25]
	v_mfma_f32_16x16x32_bf16 v[18:21], v[154:157], v[206:209], v[18:21]
	v_mfma_f32_16x16x32_bf16 v[10:13], v[146:149], v[216:219], v[10:13]
	v_mfma_f32_16x16x32_bf16 v[2:5], v[154:157], v[216:219], v[2:5]
	v_mfma_f32_16x16x32_bf16 v[66:69], v[150:153], v[186:189], v[66:69]
	v_mfma_f32_16x16x32_bf16 v[70:73], v[158:161], v[186:189], v[70:73]
	v_mfma_f32_16x16x32_bf16 v[38:41], v[150:153], v[202:205], v[38:41]
	v_mfma_f32_16x16x32_bf16 v[34:37], v[158:161], v[202:205], v[34:37]
	v_mfma_f32_16x16x32_bf16 v[22:25], v[150:153], v[212:215], v[22:25]
	v_mfma_f32_16x16x32_bf16 v[18:21], v[158:161], v[212:215], v[18:21]
	v_mfma_f32_16x16x32_bf16 v[10:13], v[150:153], v[220:223], v[10:13]
	v_mfma_f32_16x16x32_bf16 v[2:5], v[158:161], v[220:223], v[2:5]
	s_setprio 0
	s_barrier
	s_add_i32 s33, 0, 0x18000
	s_add_i32 s96, 0, 0x1c000
	v_add_u32_e32 v142, s33, v190
	v_add_u32_e32 v158, s96, v190
	ds_read_b128 v[130:133], v142
	ds_read_b128 v[134:137], v142 offset:1024
	ds_read_b128 v[138:141], v142 offset:2048
	ds_read_b128 v[142:145], v142 offset:3072
	ds_read_b128 v[146:149], v158
	ds_read_b128 v[150:153], v158 offset:1024
	ds_read_b128 v[154:157], v158 offset:2048
	ds_read_b128 v[158:161], v158 offset:3072
	s_add_u32 s0, s58, s14
	s_addc_u32 s1, s59, s15
	s_mov_b32 m0, s71
	v_lshl_add_u64 v[236:237], s[0:1], 0, v[166:167]
	ds_read_b128 v[162:165], v195 offset:32768
	ds_read_b128 v[186:189], v195 offset:33792
	ds_read_b128 v[198:201], v195 offset:34816
	ds_read_b128 v[202:205], v195 offset:35840
	ds_read_b128 v[206:209], v195 offset:36864
	ds_read_b128 v[212:215], v195 offset:37888
	ds_read_b128 v[216:219], v195 offset:38912
	ds_read_b128 v[220:223], v195 offset:39936
	global_load_lds_dwordx4 v[236:237], off
	v_lshl_add_u64 v[236:237], s[0:1], 0, v[170:171]
	s_mov_b32 m0, s73
	s_nop 0
	global_load_lds_dwordx4 v[236:237], off
	s_mov_b32 m0, s67
	s_nop 0
	global_load_lds_dwordx4 v[232:233], off
	s_mov_b32 m0, s69
	s_nop 0
	global_load_lds_dwordx4 v[234:235], off
	s_waitcnt vmcnt(8)
	s_waitcnt lgkmcnt(0)
	s_barrier
	s_setprio 1
	s_waitcnt lgkmcnt(0)
	v_mfma_f32_16x16x32_bf16 v[126:129], v[130:133], v[162:165], v[126:129]
	v_mfma_f32_16x16x32_bf16 v[122:125], v[138:141], v[162:165], v[122:125]
	v_mfma_f32_16x16x32_bf16 v[58:61], v[130:133], v[198:201], v[58:61]
	v_mfma_f32_16x16x32_bf16 v[62:65], v[138:141], v[198:201], v[62:65]
	v_mfma_f32_16x16x32_bf16 v[106:109], v[130:133], v[206:209], v[106:109]
	v_mfma_f32_16x16x32_bf16 v[110:113], v[138:141], v[206:209], v[110:113]
	v_mfma_f32_16x16x32_bf16 v[98:101], v[130:133], v[216:219], v[98:101]
	v_mfma_f32_16x16x32_bf16 v[102:105], v[138:141], v[216:219], v[102:105]
	v_mfma_f32_16x16x32_bf16 v[126:129], v[134:137], v[186:189], v[126:129]
	v_mfma_f32_16x16x32_bf16 v[122:125], v[142:145], v[186:189], v[122:125]
	v_mfma_f32_16x16x32_bf16 v[58:61], v[134:137], v[202:205], v[58:61]
	v_mfma_f32_16x16x32_bf16 v[62:65], v[142:145], v[202:205], v[62:65]
	v_mfma_f32_16x16x32_bf16 v[106:109], v[134:137], v[212:215], v[106:109]
	v_mfma_f32_16x16x32_bf16 v[110:113], v[142:145], v[212:215], v[110:113]
	v_mfma_f32_16x16x32_bf16 v[98:101], v[134:137], v[220:223], v[98:101]
	v_mfma_f32_16x16x32_bf16 v[102:105], v[142:145], v[220:223], v[102:105]
	s_setprio 0
	s_setprio 1
	v_mfma_f32_16x16x32_bf16 v[118:121], v[146:149], v[162:165], v[118:121]
	v_mfma_f32_16x16x32_bf16 v[114:117], v[154:157], v[162:165], v[114:117]
	v_mfma_f32_16x16x32_bf16 v[50:53], v[146:149], v[198:201], v[50:53]
	v_mfma_f32_16x16x32_bf16 v[54:57], v[154:157], v[198:201], v[54:57]
	v_mfma_f32_16x16x32_bf16 v[90:93], v[146:149], v[206:209], v[90:93]
	v_mfma_f32_16x16x32_bf16 v[94:97], v[154:157], v[206:209], v[94:97]
	v_mfma_f32_16x16x32_bf16 v[74:77], v[146:149], v[216:219], v[74:77]
	v_mfma_f32_16x16x32_bf16 v[78:81], v[154:157], v[216:219], v[78:81]
	v_mfma_f32_16x16x32_bf16 v[118:121], v[150:153], v[186:189], v[118:121]
	v_mfma_f32_16x16x32_bf16 v[114:117], v[158:161], v[186:189], v[114:117]
	v_mfma_f32_16x16x32_bf16 v[50:53], v[150:153], v[202:205], v[50:53]
	v_mfma_f32_16x16x32_bf16 v[54:57], v[158:161], v[202:205], v[54:57]
	v_mfma_f32_16x16x32_bf16 v[90:93], v[150:153], v[212:215], v[90:93]
	v_mfma_f32_16x16x32_bf16 v[94:97], v[158:161], v[212:215], v[94:97]
	v_mfma_f32_16x16x32_bf16 v[74:77], v[150:153], v[220:223], v[74:77]
	v_mfma_f32_16x16x32_bf16 v[78:81], v[158:161], v[220:223], v[78:81]
	s_setprio 0
	s_barrier
; #define PG8_STAGE(bufoff, gbase, voff) do { _Pragma("unroll") for (int _i = 0; _i < 2; ++_i) \
;         __builtin_amdgcn_global_load_lds((const unsigned*)((const char*)(gbase) + (voff)[_i]), (PG8_LAS unsigned*)(lds + (bufoff) + ldsw + _i * 8192), 16, 0, 0); } while (0)
; #define PG8_LDA(dst, b, h) do { _Pragma("unroll") for (int m = 0; m < 4; ++m) { const bf16x8 f0_ = *(const PG8_LAS bf16x8*)(lds + PG8_SA(b, h) + aoff + m * 2048), f1_ = *(const PG8_LAS bf16x8*)(lds + PG8_SA(b, h) + aoff + m * 2048 + 1024); dst[m].set(f0_, f1_); } } while (0)
; #define PG8_WAIT_V(n) asm volatile("s_waitcnt vmcnt(" #n ")" ::: "memory")
; #define PG8_WAIT_L(n) asm volatile("s_waitcnt lgkmcnt(" #n ")" ::: "memory")
; #define PG8_BAR __builtin_amdgcn_s_barrier()
; #define PG8_SCHED __builtin_amdgcn_sched_barrier(0)
; template <class Epi, class Sched, bool ALIGN_EPI = false, bool SP2 = false>
; __device__ __forceinline__ void gemm_phase(PG8_LAS unsigned char* lds, const Gemm g, const Sched& S, const Epi& E) {
;     ...
;         for (int t = 0; t < nt; t += 2) {
;             if constexpr (Epi::MIDK) { if (t == (nt >> 1)) E.mid(acc, cur, wr, wc, fr, fq); }
;             const bool last = (t == nt - 2);
;             const char* a1 = cA + (size_t)(t + 1) * kstep;
;             const char* a2 = last ? nA : cA + (size_t)(t + 2) * kstep; const char* b2 = last ? nB : cB + (size_t)(t + 2) * kstep;
;             const char* a3 = a2 + kstep; const char* b3 = b2 + kstep;
;     ...
;             PG8_LDA(At, 1, 1); PG8_STAGE(PG8_SB(1, 0), b3, voffB); PG8_STAGE(PG8_SB(1, 1), b3 + hstepB, voffB); PG8_STAGE(PG8_SA(1, 0), a3, voffA);
;             PG8_WAIT_V(8); PG8_WAIT_L(0); PG8_BAR; PG8_MMA(1, 0, At, B0); PG8_MMA(1, 1, At, B1); PG8_BAR; PG8_SCHED;
	s_add_i32 s0, s33, s66
	v_lshl_add_u64 v[224:225], v[224:225], 0, s[28:29]
	s_mov_b32 m0, s0
	ds_read_b128 v[162:165], v195 offset:49152
	ds_read_b128 v[186:189], v195 offset:50176
	ds_read_b128 v[198:201], v195 offset:51200
	ds_read_b128 v[202:205], v195 offset:52224
	ds_read_b128 v[206:209], v195 offset:53248
	ds_read_b128 v[212:215], v195 offset:54272
	ds_read_b128 v[216:219], v195 offset:55296
	ds_read_b128 v[220:223], v195 offset:56320
	global_load_lds_dwordx4 v[224:225], off
	v_lshl_add_u64 v[224:225], v[226:227], 0, s[28:29]
	s_add_i32 m0, s0, 0x2000
	s_add_i32 s0, s96, s66
	global_load_lds_dwordx4 v[224:225], off
	v_lshl_add_u64 v[224:225], v[228:229], 0, s[28:29]
	s_mov_b32 m0, s0
	s_nop 0
	global_load_lds_dwordx4 v[224:225], off
	v_lshl_add_u64 v[224:225], v[230:231], 0, s[28:29]
	s_add_i32 m0, s0, 0x2000
	s_nop 0
	global_load_lds_dwordx4 v[224:225], off
	v_lshl_add_u64 v[224:225], v[232:233], 0, s[28:29]
	s_mov_b32 m0, s74
	s_nop 0
	global_load_lds_dwordx4 v[224:225], off
	v_lshl_add_u64 v[224:225], v[234:235], 0, s[28:29]
	s_mov_b32 m0, s75
	s_nop 0
	global_load_lds_dwordx4 v[224:225], off
	s_waitcnt vmcnt(6)
	s_waitcnt lgkmcnt(0)
	s_barrier
	s_setprio 1
	s_waitcnt lgkmcnt(0)
	v_mfma_f32_16x16x32_bf16 v[82:85], v[130:133], v[162:165], v[82:85]
	v_mfma_f32_16x16x32_bf16 v[86:89], v[138:141], v[162:165], v[86:89]
	v_mfma_f32_16x16x32_bf16 v[46:49], v[130:133], v[198:201], v[46:49]
	v_mfma_f32_16x16x32_bf16 v[42:45], v[138:141], v[198:201], v[42:45]
	v_mfma_f32_16x16x32_bf16 v[30:33], v[130:133], v[206:209], v[30:33]
	v_mfma_f32_16x16x32_bf16 v[26:29], v[138:141], v[206:209], v[26:29]
	v_mfma_f32_16x16x32_bf16 v[14:17], v[130:133], v[216:219], v[14:17]
	v_mfma_f32_16x16x32_bf16 v[6:9], v[138:141], v[216:219], v[6:9]
	v_mfma_f32_16x16x32_bf16 v[82:85], v[134:137], v[186:189], v[82:85]
	v_mfma_f32_16x16x32_bf16 v[86:89], v[142:145], v[186:189], v[86:89]
	v_mfma_f32_16x16x32_bf16 v[46:49], v[134:137], v[202:205], v[46:49]
	v_mfma_f32_16x16x32_bf16 v[42:45], v[142:145], v[202:205], v[42:45]
	v_mfma_f32_16x16x32_bf16 v[30:33], v[134:137], v[212:215], v[30:33]
	v_mfma_f32_16x16x32_bf16 v[26:29], v[142:145], v[212:215], v[26:29]
	v_mfma_f32_16x16x32_bf16 v[14:17], v[134:137], v[220:223], v[14:17]
	v_mfma_f32_16x16x32_bf16 v[6:9], v[142:145], v[220:223], v[6:9]
	s_setprio 0
	s_setprio 1
	v_mfma_f32_16x16x32_bf16 v[66:69], v[146:149], v[162:165], v[66:69]
	v_mfma_f32_16x16x32_bf16 v[70:73], v[154:157], v[162:165], v[70:73]
	v_mfma_f32_16x16x32_bf16 v[38:41], v[146:149], v[198:201], v[38:41]
	v_mfma_f32_16x16x32_bf16 v[34:37], v[154:157], v[198:201], v[34:37]
	v_mfma_f32_16x16x32_bf16 v[22:25], v[146:149], v[206:209], v[22:25]
	v_mfma_f32_16x16x32_bf16 v[18:21], v[154:157], v[206:209], v[18:21]
	v_mfma_f32_16x16x32_bf16 v[10:13], v[146:149], v[216:219], v[10:13]
	v_mfma_f32_16x16x32_bf16 v[2:5], v[154:157], v[216:219], v[2:5]
	v_mfma_f32_16x16x32_bf16 v[66:69], v[150:153], v[186:189], v[66:69]
	v_mfma_f32_16x16x32_bf16 v[70:73], v[158:161], v[186:189], v[70:73]
	v_mfma_f32_16x16x32_bf16 v[38:41], v[150:153], v[202:205], v[38:41]
	v_mfma_f32_16x16x32_bf16 v[34:37], v[158:161], v[202:205], v[34:37]
	v_mfma_f32_16x16x32_bf16 v[22:25], v[150:153], v[212:215], v[22:25]
	v_mfma_f32_16x16x32_bf16 v[18:21], v[158:161], v[212:215], v[18:21]
	v_mfma_f32_16x16x32_bf16 v[10:13], v[150:153], v[220:223], v[10:13]
	v_mfma_f32_16x16x32_bf16 v[2:5], v[158:161], v[220:223], v[2:5]
	s_setprio 0
	s_barrier
	s_add_u32 s56, s56, 0x100
	s_addc_u32 s57, s57, 0
	s_add_u32 s93, s93, 0x100
	s_addc_u32 s94, s94, 0
	s_cmp_ge_i32 s95, s76
	s_mov_b32 s58, s95
	s_cbranch_scc0 .LBB0_1070
	v_readlane_b32 s94, v254, 5
	v_readlane_b32 s95, v254, 6

; #define PG8_STAGE(bufoff, gbase, voff) do { _Pragma("unroll") for (int _i = 0; _i < 2; ++_i) \
;         __builtin_amdgcn_global_load_lds((const unsigned*)((const char*)(gbase) + (voff)[_i]), (PG8_LAS unsigned*)(lds + (bufoff) + ldsw + _i * 8192), 16, 0, 0); } while (0)
; #define PG8_LDA(dst, b, h) do { _Pragma("unroll") for (int m = 0; m < 4; ++m) { const bf16x8 f0_ = *(const PG8_LAS bf16x8*)(lds + PG8_SA(b, h) + aoff + m * 2048), f1_ = *(const PG8_LAS bf16x8*)(lds + PG8_SA(b, h) + aoff + m * 2048 + 1024); dst[m].set(f0_, f1_); } } while (0)
; #define PG8_LDB(dst, b, h) do { _Pragma("unroll") for (int n = 0; n < 2; ++n) { const bf16x8 f0_ = *(const PG8_LAS bf16x8*)(lds + PG8_SB(b, h) + boff + n * 2048), f1_ = *(const PG8_LAS bf16x8*)(lds + PG8_SB(b, h) + boff + n * 2048 + 1024); dst[n].set(f0_, f1_); } } while (0)
; #define PG8_WAIT_V(n) asm volatile("s_waitcnt vmcnt(" #n ")" ::: "memory")
; #define PG8_WAIT_L(n) asm volatile("s_waitcnt lgkmcnt(" #n ")" ::: "memory")
; #define PG8_BAR __builtin_amdgcn_s_barrier()
; #define PG8_SCHED __builtin_amdgcn_sched_barrier(0)
; template <class Epi, class Sched, bool ALIGN_EPI = false, bool SP2 = false>
; __device__ __forceinline__ void gemm_phase(PG8_LAS unsigned char* lds, const Gemm g, const Sched& S, const Epi& E) {
;     ...
;             PG8_LDB(B0, 0, 0); PG8_LDB(B1, 0, 1); PG8_SCHED; PG8_LDA(At, 0, 0); PG8_STAGE(PG8_SA(1, 1), a1 + hstep, voffA);
;             PG8_WAIT_V(8); PG8_WAIT_L(0); PG8_BAR; PG8_MMA(0, 0, At, B0); PG8_MMA(0, 1, At, B1); PG8_BAR; PG8_SCHED;
;             PG8_LDA(At, 0, 1); PG8_STAGE(PG8_SB(0, 0), b2, voffB); PG8_STAGE(PG8_SB(0, 1), b2 + hstepB, voffB); PG8_STAGE(PG8_SA(0, 0), a2, voffA);
;             PG8_WAIT_V(8); PG8_WAIT_L(0); PG8_BAR; PG8_MMA(1, 0, At, B0); PG8_MMA(1, 1, At, B1); PG8_BAR; PG8_SCHED;
.LBB0_1171:
	ds_read_b128 v[156:159], v152
	ds_read_b128 v[160:163], v152 offset:1024
	ds_read_b128 v[164:167], v152 offset:2048
	ds_read_b128 v[168:171], v152 offset:3072
	ds_read_b128 v[172:175], v153
	ds_read_b128 v[176:179], v153 offset:1024
	ds_read_b128 v[180:183], v153 offset:2048
	ds_read_b128 v[184:187], v153 offset:3072
	s_add_i32 s61, s34, 2
	s_add_u32 s0, s30, 0x80
	s_addc_u32 s1, s31, 0
	s_cmp_eq_u32 s49, s34
	s_cselect_b32 s34, s6, s0
	s_cselect_b32 s35, s7, s1
	s_cselect_b32 s1, s29, s59
	s_cselect_b32 s0, s28, s58
	v_lshl_add_u64 v[148:149], s[30:31], 0, v[140:141]
	s_add_i32 m0, s40, 0xc000
	ds_read_b128 v[188:191], v154
	ds_read_b128 v[192:195], v154 offset:1024
	ds_read_b128 v[196:199], v154 offset:2048
	ds_read_b128 v[200:203], v154 offset:3072
	ds_read_b128 v[204:207], v154 offset:4096
	ds_read_b128 v[212:215], v154 offset:5120
	ds_read_b128 v[216:219], v154 offset:6144
	ds_read_b128 v[220:223], v154 offset:7168
	global_load_lds_dwordx4 v[148:149], off
	v_lshl_add_u64 v[148:149], s[30:31], 0, v[142:143]
	s_add_i32 m0, s40, 0xe000
	s_nop 0
	global_load_lds_dwordx4 v[148:149], off
	s_waitcnt vmcnt(8)
	s_waitcnt lgkmcnt(0)
	s_barrier
	s_setprio 1
	s_waitcnt lgkmcnt(0)
	v_mfma_f32_16x16x32_bf16 v[126:129], v[156:159], v[188:191], v[126:129]
	v_mfma_f32_16x16x32_bf16 v[122:125], v[164:167], v[188:191], v[122:125]
	v_mfma_f32_16x16x32_bf16 v[110:113], v[156:159], v[196:199], v[110:113]
	v_mfma_f32_16x16x32_bf16 v[106:109], v[164:167], v[196:199], v[106:109]
	v_mfma_f32_16x16x32_bf16 v[94:97], v[156:159], v[204:207], v[94:97]
	v_mfma_f32_16x16x32_bf16 v[90:93], v[164:167], v[204:207], v[90:93]
	v_mfma_f32_16x16x32_bf16 v[78:81], v[156:159], v[216:219], v[78:81]
	v_mfma_f32_16x16x32_bf16 v[74:77], v[164:167], v[216:219], v[74:77]
	v_mfma_f32_16x16x32_bf16 v[126:129], v[160:163], v[192:195], v[126:129]
	v_mfma_f32_16x16x32_bf16 v[122:125], v[168:171], v[192:195], v[122:125]
	v_mfma_f32_16x16x32_bf16 v[110:113], v[160:163], v[200:203], v[110:113]
	v_mfma_f32_16x16x32_bf16 v[106:109], v[168:171], v[200:203], v[106:109]
	v_mfma_f32_16x16x32_bf16 v[94:97], v[160:163], v[212:215], v[94:97]
	v_mfma_f32_16x16x32_bf16 v[90:93], v[168:171], v[212:215], v[90:93]
	v_mfma_f32_16x16x32_bf16 v[78:81], v[160:163], v[220:223], v[78:81]
	v_mfma_f32_16x16x32_bf16 v[74:77], v[168:171], v[220:223], v[74:77]
	s_setprio 0
	s_setprio 1
	v_mfma_f32_16x16x32_bf16 v[118:121], v[172:175], v[188:191], v[118:121]
	v_mfma_f32_16x16x32_bf16 v[114:117], v[180:183], v[188:191], v[114:117]
	v_mfma_f32_16x16x32_bf16 v[102:105], v[172:175], v[196:199], v[102:105]
	v_mfma_f32_16x16x32_bf16 v[98:101], v[180:183], v[196:199], v[98:101]
	v_mfma_f32_16x16x32_bf16 v[86:89], v[172:175], v[204:207], v[86:89]
	v_mfma_f32_16x16x32_bf16 v[82:85], v[180:183], v[204:207], v[82:85]
	v_mfma_f32_16x16x32_bf16 v[70:73], v[172:175], v[216:219], v[70:73]
	v_mfma_f32_16x16x32_bf16 v[66:69], v[180:183], v[216:219], v[66:69]
	v_mfma_f32_16x16x32_bf16 v[118:121], v[176:179], v[192:195], v[118:121]
	v_mfma_f32_16x16x32_bf16 v[114:117], v[184:187], v[192:195], v[114:117]
	v_mfma_f32_16x16x32_bf16 v[102:105], v[176:179], v[200:203], v[102:105]
	v_mfma_f32_16x16x32_bf16 v[98:101], v[184:187], v[200:203], v[98:101]
	v_mfma_f32_16x16x32_bf16 v[86:89], v[176:179], v[212:215], v[86:89]
	v_mfma_f32_16x16x32_bf16 v[82:85], v[184:187], v[212:215], v[82:85]
	v_mfma_f32_16x16x32_bf16 v[70:73], v[176:179], v[220:223], v[70:73]
	v_mfma_f32_16x16x32_bf16 v[66:69], v[184:187], v[220:223], v[66:69]
	s_setprio 0
	s_barrier
	s_add_i32 s33, s52, s39
	v_lshl_add_u64 v[148:149], s[0:1], 0, v[132:133]
	s_mov_b32 m0, s33
	ds_read_b128 v[188:191], v154 offset:16384
	ds_read_b128 v[192:195], v154 offset:17408
	ds_read_b128 v[196:199], v154 offset:18432
	ds_read_b128 v[200:203], v154 offset:19456
	ds_read_b128 v[204:207], v154 offset:20480
	ds_read_b128 v[212:215], v154 offset:21504
	ds_read_b128 v[216:219], v154 offset:22528
	ds_read_b128 v[220:223], v154 offset:23552
	global_load_lds_dwordx4 v[148:149], off
	s_add_i32 m0, s33, 0x2000
	v_lshl_add_u64 v[208:209], s[0:1], 0, v[136:137]
	s_add_u32 s0, s0, s14
	s_addc_u32 s1, s1, s15
	s_add_i32 s33, s53, s39
	global_load_lds_dwordx4 v[208:209], off
	v_lshl_add_u64 v[224:225], s[0:1], 0, v[132:133]
	s_mov_b32 m0, s33
	v_lshl_add_u64 v[226:227], s[0:1], 0, v[136:137]
	global_load_lds_dwordx4 v[224:225], off
	s_add_i32 m0, s33, 0x2000
	v_lshl_add_u64 v[228:229], s[34:35], 0, v[130:131]
	global_load_lds_dwordx4 v[226:227], off
	v_lshl_add_u64 v[230:231], s[34:35], 0, v[134:135]
	s_waitcnt vmcnt(6)
	s_waitcnt lgkmcnt(0)
	s_barrier
; #define PG8_STAGE(bufoff, gbase, voff) do { _Pragma("unroll") for (int _i = 0; _i < 2; ++_i) \
;         __builtin_amdgcn_global_load_lds((const unsigned*)((const char*)(gbase) + (voff)[_i]), (PG8_LAS unsigned*)(lds + (bufoff) + ldsw + _i * 8192), 16, 0, 0); } while (0)
; #define PG8_LDA(dst, b, h) do { _Pragma("unroll") for (int m = 0; m < 4; ++m) { const bf16x8 f0_ = *(const PG8_LAS bf16x8*)(lds + PG8_SA(b, h) + aoff + m * 2048), f1_ = *(const PG8_LAS bf16x8*)(lds + PG8_SA(b, h) + aoff + m * 2048 + 1024); dst[m].set(f0_, f1_); } } while (0)
; #define PG8_LDB(dst, b, h) do { _Pragma("unroll") for (int n = 0; n < 2; ++n) { const bf16x8 f0_ = *(const PG8_LAS bf16x8*)(lds + PG8_SB(b, h) + boff + n * 2048), f1_ = *(const PG8_LAS bf16x8*)(lds + PG8_SB(b, h) + boff + n * 2048 + 1024); dst[n].set(f0_, f1_); } } while (0)
; #define PG8_WAIT_V(n) asm volatile("s_waitcnt vmcnt(" #n ")" ::: "memory")
; #define PG8_WAIT_L(n) asm volatile("s_waitcnt lgkmcnt(" #n ")" ::: "memory")
; #define PG8_BAR __builtin_amdgcn_s_barrier()
; #define PG8_SCHED __builtin_amdgcn_sched_barrier(0)
; template <class Epi, class Sched, bool ALIGN_EPI = false, bool SP2 = false>
; __device__ __forceinline__ void gemm_phase(PG8_LAS unsigned char* lds, const Gemm g, const Sched& S, const Epi& E) {
;     ...
;             PG8_WAIT_V(8); PG8_WAIT_L(0); PG8_BAR; PG8_MMA(1, 0, At, B0); PG8_MMA(1, 1, At, B1); PG8_BAR; PG8_SCHED;
;             PG8_LDB(B0, 1, 0); PG8_LDB(B1, 1, 1); PG8_SCHED; PG8_LDA(At, 1, 0); PG8_STAGE(PG8_SA(0, 1), a2 + hstep, voffA);
;             PG8_WAIT_V(8); PG8_WAIT_L(0); PG8_BAR; PG8_MMA(0, 0, At, B0); PG8_MMA(0, 1, At, B1); PG8_BAR; PG8_SCHED;
	s_setprio 1
	s_waitcnt lgkmcnt(0)
	v_mfma_f32_16x16x32_bf16 v[62:65], v[156:159], v[188:191], v[62:65]
	v_mfma_f32_16x16x32_bf16 v[58:61], v[164:167], v[188:191], v[58:61]
	v_mfma_f32_16x16x32_bf16 v[46:49], v[156:159], v[196:199], v[46:49]
	v_mfma_f32_16x16x32_bf16 v[42:45], v[164:167], v[196:199], v[42:45]
	v_mfma_f32_16x16x32_bf16 v[30:33], v[156:159], v[204:207], v[30:33]
	v_mfma_f32_16x16x32_bf16 v[26:29], v[164:167], v[204:207], v[26:29]
	v_mfma_f32_16x16x32_bf16 v[14:17], v[156:159], v[216:219], v[14:17]
	v_mfma_f32_16x16x32_bf16 v[6:9], v[164:167], v[216:219], v[6:9]
	v_mfma_f32_16x16x32_bf16 v[62:65], v[160:163], v[192:195], v[62:65]
	v_mfma_f32_16x16x32_bf16 v[58:61], v[168:171], v[192:195], v[58:61]
	v_mfma_f32_16x16x32_bf16 v[46:49], v[160:163], v[200:203], v[46:49]
	v_mfma_f32_16x16x32_bf16 v[42:45], v[168:171], v[200:203], v[42:45]
	v_mfma_f32_16x16x32_bf16 v[30:33], v[160:163], v[212:215], v[30:33]
	v_mfma_f32_16x16x32_bf16 v[26:29], v[168:171], v[212:215], v[26:29]
	v_mfma_f32_16x16x32_bf16 v[14:17], v[160:163], v[220:223], v[14:17]
	v_mfma_f32_16x16x32_bf16 v[6:9], v[168:171], v[220:223], v[6:9]
	s_setprio 0
	s_setprio 1
	v_mfma_f32_16x16x32_bf16 v[54:57], v[172:175], v[188:191], v[54:57]
	v_mfma_f32_16x16x32_bf16 v[50:53], v[180:183], v[188:191], v[50:53]
	v_mfma_f32_16x16x32_bf16 v[38:41], v[172:175], v[196:199], v[38:41]
	v_mfma_f32_16x16x32_bf16 v[34:37], v[180:183], v[196:199], v[34:37]
	v_mfma_f32_16x16x32_bf16 v[22:25], v[172:175], v[204:207], v[22:25]
	v_mfma_f32_16x16x32_bf16 v[18:21], v[180:183], v[204:207], v[18:21]
	v_mfma_f32_16x16x32_bf16 v[10:13], v[172:175], v[216:219], v[10:13]
	v_mfma_f32_16x16x32_bf16 v[2:5], v[180:183], v[216:219], v[2:5]
	v_mfma_f32_16x16x32_bf16 v[54:57], v[176:179], v[192:195], v[54:57]
	v_mfma_f32_16x16x32_bf16 v[50:53], v[184:187], v[192:195], v[50:53]
	v_mfma_f32_16x16x32_bf16 v[38:41], v[176:179], v[200:203], v[38:41]
	v_mfma_f32_16x16x32_bf16 v[34:37], v[184:187], v[200:203], v[34:37]
	v_mfma_f32_16x16x32_bf16 v[22:25], v[176:179], v[212:215], v[22:25]
	v_mfma_f32_16x16x32_bf16 v[18:21], v[184:187], v[212:215], v[18:21]
	v_mfma_f32_16x16x32_bf16 v[10:13], v[176:179], v[220:223], v[10:13]
	v_mfma_f32_16x16x32_bf16 v[2:5], v[184:187], v[220:223], v[2:5]
	s_setprio 0
	s_barrier
	s_add_i32 s33, 0, 0x18000
	s_add_i32 s63, 0, 0x1c000
	v_add_u32_e32 v168, s33, v1
	v_add_u32_e32 v184, s63, v1
	ds_read_b128 v[156:159], v168
	ds_read_b128 v[160:163], v168 offset:1024
	ds_read_b128 v[164:167], v168 offset:2048
	ds_read_b128 v[168:171], v168 offset:3072
	ds_read_b128 v[172:175], v184
	ds_read_b128 v[176:179], v184 offset:1024
	ds_read_b128 v[180:183], v184 offset:2048
	ds_read_b128 v[184:187], v184 offset:3072
	s_add_u32 s0, s34, s12
	s_addc_u32 s1, s35, s13
	s_mov_b32 m0, s42
	v_lshl_add_u64 v[232:233], s[0:1], 0, v[130:131]
	ds_read_b128 v[188:191], v154 offset:32768
	ds_read_b128 v[192:195], v154 offset:33792
	ds_read_b128 v[196:199], v154 offset:34816
	ds_read_b128 v[200:203], v154 offset:35840
	ds_read_b128 v[204:207], v154 offset:36864
	ds_read_b128 v[212:215], v154 offset:37888
	ds_read_b128 v[216:219], v154 offset:38912
	ds_read_b128 v[220:223], v154 offset:39936
	global_load_lds_dwordx4 v[232:233], off
	v_lshl_add_u64 v[232:233], s[0:1], 0, v[134:135]
	s_mov_b32 m0, s43
	s_nop 0
	global_load_lds_dwordx4 v[232:233], off
	s_mov_b32 m0, s40
	s_nop 0
	global_load_lds_dwordx4 v[228:229], off
	s_mov_b32 m0, s41
	s_nop 0
	global_load_lds_dwordx4 v[230:231], off
	s_waitcnt vmcnt(8)
	s_waitcnt lgkmcnt(0)
	s_barrier
	s_setprio 1
	s_waitcnt lgkmcnt(0)
	v_mfma_f32_16x16x32_bf16 v[126:129], v[156:159], v[188:191], v[126:129]
	v_mfma_f32_16x16x32_bf16 v[122:125], v[164:167], v[188:191], v[122:125]
	v_mfma_f32_16x16x32_bf16 v[110:113], v[156:159], v[196:199], v[110:113]
	v_mfma_f32_16x16x32_bf16 v[106:109], v[164:167], v[196:199], v[106:109]
	v_mfma_f32_16x16x32_bf16 v[94:97], v[156:159], v[204:207], v[94:97]
	v_mfma_f32_16x16x32_bf16 v[90:93], v[164:167], v[204:207], v[90:93]
	v_mfma_f32_16x16x32_bf16 v[78:81], v[156:159], v[216:219], v[78:81]
	v_mfma_f32_16x16x32_bf16 v[74:77], v[164:167], v[216:219], v[74:77]
	v_mfma_f32_16x16x32_bf16 v[126:129], v[160:163], v[192:195], v[126:129]
	v_mfma_f32_16x16x32_bf16 v[122:125], v[168:171], v[192:195], v[122:125]
	v_mfma_f32_16x16x32_bf16 v[110:113], v[160:163], v[200:203], v[110:113]
	v_mfma_f32_16x16x32_bf16 v[106:109], v[168:171], v[200:203], v[106:109]
	v_mfma_f32_16x16x32_bf16 v[94:97], v[160:163], v[212:215], v[94:97]
	v_mfma_f32_16x16x32_bf16 v[90:93], v[168:171], v[212:215], v[90:93]
	v_mfma_f32_16x16x32_bf16 v[78:81], v[160:163], v[220:223], v[78:81]
	v_mfma_f32_16x16x32_bf16 v[74:77], v[168:171], v[220:223], v[74:77]
	s_setprio 0
	s_setprio 1
	v_mfma_f32_16x16x32_bf16 v[118:121], v[172:175], v[188:191], v[118:121]
	v_mfma_f32_16x16x32_bf16 v[114:117], v[180:183], v[188:191], v[114:117]
	v_mfma_f32_16x16x32_bf16 v[102:105], v[172:175], v[196:199], v[102:105]
	v_mfma_f32_16x16x32_bf16 v[98:101], v[180:183], v[196:199], v[98:101]
	v_mfma_f32_16x16x32_bf16 v[86:89], v[172:175], v[204:207], v[86:89]
	v_mfma_f32_16x16x32_bf16 v[82:85], v[180:183], v[204:207], v[82:85]
	v_mfma_f32_16x16x32_bf16 v[70:73], v[172:175], v[216:219], v[70:73]
	v_mfma_f32_16x16x32_bf16 v[66:69], v[180:183], v[216:219], v[66:69]
	v_mfma_f32_16x16x32_bf16 v[118:121], v[176:179], v[192:195], v[118:121]
	v_mfma_f32_16x16x32_bf16 v[114:117], v[184:187], v[192:195], v[114:117]
	v_mfma_f32_16x16x32_bf16 v[102:105], v[176:179], v[200:203], v[102:105]
	v_mfma_f32_16x16x32_bf16 v[98:101], v[184:187], v[200:203], v[98:101]
	v_mfma_f32_16x16x32_bf16 v[86:89], v[176:179], v[212:215], v[86:89]
	v_mfma_f32_16x16x32_bf16 v[82:85], v[184:187], v[212:215], v[82:85]
	v_mfma_f32_16x16x32_bf16 v[70:73], v[176:179], v[220:223], v[70:73]
	v_mfma_f32_16x16x32_bf16 v[66:69], v[184:187], v[220:223], v[66:69]
	s_setprio 0
	s_barrier
; #define PG8_STAGE(bufoff, gbase, voff) do { _Pragma("unroll") for (int _i = 0; _i < 2; ++_i) \
;         __builtin_amdgcn_global_load_lds((const unsigned*)((const char*)(gbase) + (voff)[_i]), (PG8_LAS unsigned*)(lds + (bufoff) + ldsw + _i * 8192), 16, 0, 0); } while (0)
; #define PG8_LDA(dst, b, h) do { _Pragma("unroll") for (int m = 0; m < 4; ++m) { const bf16x8 f0_ = *(const PG8_LAS bf16x8*)(lds + PG8_SA(b, h) + aoff + m * 2048), f1_ = *(const PG8_LAS bf16x8*)(lds + PG8_SA(b, h) + aoff + m * 2048 + 1024); dst[m].set(f0_, f1_); } } while (0)
; #define PG8_WAIT_V(n) asm volatile("s_waitcnt vmcnt(" #n ")" ::: "memory")
; #define PG8_WAIT_L(n) asm volatile("s_waitcnt lgkmcnt(" #n ")" ::: "memory")
; #define PG8_BAR __builtin_amdgcn_s_barrier()
; #define PG8_SCHED __builtin_amdgcn_sched_barrier(0)
; template <class Epi, class Sched, bool ALIGN_EPI = false, bool SP2 = false>
; __device__ __forceinline__ void gemm_phase(PG8_LAS unsigned char* lds, const Gemm g, const Sched& S, const Epi& E) {
;     ...
;             PG8_LDA(At, 1, 1); PG8_STAGE(PG8_SB(1, 0), b3, voffB); PG8_STAGE(PG8_SB(1, 1), b3 + hstepB, voffB); PG8_STAGE(PG8_SA(1, 0), a3, voffA);
;             PG8_WAIT_V(8); PG8_WAIT_L(0); PG8_BAR; PG8_MMA(1, 0, At, B0); PG8_MMA(1, 1, At, B1); PG8_BAR; PG8_SCHED;
	s_add_i32 s0, s33, s39
	v_lshl_add_u64 v[148:149], v[148:149], 0, s[22:23]
	s_mov_b32 m0, s0
	ds_read_b128 v[188:191], v154 offset:49152
	ds_read_b128 v[192:195], v154 offset:50176
	ds_read_b128 v[196:199], v154 offset:51200
	ds_read_b128 v[200:203], v154 offset:52224
	ds_read_b128 v[204:207], v154 offset:53248
	ds_read_b128 v[212:215], v154 offset:54272
	ds_read_b128 v[216:219], v154 offset:55296
	ds_read_b128 v[220:223], v154 offset:56320
	global_load_lds_dwordx4 v[148:149], off
	v_lshl_add_u64 v[148:149], v[208:209], 0, s[22:23]
	s_add_i32 m0, s0, 0x2000
	s_add_i32 s0, s63, s39
	global_load_lds_dwordx4 v[148:149], off
	v_lshl_add_u64 v[148:149], v[224:225], 0, s[22:23]
	s_mov_b32 m0, s0
	s_nop 0
	global_load_lds_dwordx4 v[148:149], off
	v_lshl_add_u64 v[148:149], v[226:227], 0, s[22:23]
	s_add_i32 m0, s0, 0x2000
	s_nop 0
	global_load_lds_dwordx4 v[148:149], off
	v_lshl_add_u64 v[148:149], v[228:229], 0, s[22:23]
	s_mov_b32 m0, s45
	s_nop 0
	global_load_lds_dwordx4 v[148:149], off
	v_lshl_add_u64 v[148:149], v[230:231], 0, s[22:23]
	s_mov_b32 m0, s46
	s_nop 0
	global_load_lds_dwordx4 v[148:149], off
	s_waitcnt vmcnt(6)
	s_waitcnt lgkmcnt(0)
	s_barrier
	s_setprio 1
	s_waitcnt lgkmcnt(0)
	v_mfma_f32_16x16x32_bf16 v[62:65], v[156:159], v[188:191], v[62:65]
	v_mfma_f32_16x16x32_bf16 v[58:61], v[164:167], v[188:191], v[58:61]
	v_mfma_f32_16x16x32_bf16 v[46:49], v[156:159], v[196:199], v[46:49]
	v_mfma_f32_16x16x32_bf16 v[42:45], v[164:167], v[196:199], v[42:45]
	v_mfma_f32_16x16x32_bf16 v[30:33], v[156:159], v[204:207], v[30:33]
	v_mfma_f32_16x16x32_bf16 v[26:29], v[164:167], v[204:207], v[26:29]
	v_mfma_f32_16x16x32_bf16 v[14:17], v[156:159], v[216:219], v[14:17]
	v_mfma_f32_16x16x32_bf16 v[6:9], v[164:167], v[216:219], v[6:9]
	v_mfma_f32_16x16x32_bf16 v[62:65], v[160:163], v[192:195], v[62:65]
	v_mfma_f32_16x16x32_bf16 v[58:61], v[168:171], v[192:195], v[58:61]
	v_mfma_f32_16x16x32_bf16 v[46:49], v[160:163], v[200:203], v[46:49]
	v_mfma_f32_16x16x32_bf16 v[42:45], v[168:171], v[200:203], v[42:45]
	v_mfma_f32_16x16x32_bf16 v[30:33], v[160:163], v[212:215], v[30:33]
	v_mfma_f32_16x16x32_bf16 v[26:29], v[168:171], v[212:215], v[26:29]
	v_mfma_f32_16x16x32_bf16 v[14:17], v[160:163], v[220:223], v[14:17]
	v_mfma_f32_16x16x32_bf16 v[6:9], v[168:171], v[220:223], v[6:9]
	s_setprio 0
	s_setprio 1
	v_mfma_f32_16x16x32_bf16 v[54:57], v[172:175], v[188:191], v[54:57]
	v_mfma_f32_16x16x32_bf16 v[50:53], v[180:183], v[188:191], v[50:53]
	v_mfma_f32_16x16x32_bf16 v[38:41], v[172:175], v[196:199], v[38:41]
	v_mfma_f32_16x16x32_bf16 v[34:37], v[180:183], v[196:199], v[34:37]
	v_mfma_f32_16x16x32_bf16 v[22:25], v[172:175], v[204:207], v[22:25]
	v_mfma_f32_16x16x32_bf16 v[18:21], v[180:183], v[204:207], v[18:21]
	v_mfma_f32_16x16x32_bf16 v[10:13], v[172:175], v[216:219], v[10:13]
	v_mfma_f32_16x16x32_bf16 v[2:5], v[180:183], v[216:219], v[2:5]
	v_mfma_f32_16x16x32_bf16 v[54:57], v[176:179], v[192:195], v[54:57]
	v_mfma_f32_16x16x32_bf16 v[50:53], v[184:187], v[192:195], v[50:53]
	v_mfma_f32_16x16x32_bf16 v[38:41], v[176:179], v[200:203], v[38:41]
	v_mfma_f32_16x16x32_bf16 v[34:37], v[184:187], v[200:203], v[34:37]
	v_mfma_f32_16x16x32_bf16 v[22:25], v[176:179], v[212:215], v[22:25]
	v_mfma_f32_16x16x32_bf16 v[18:21], v[184:187], v[212:215], v[18:21]
	v_mfma_f32_16x16x32_bf16 v[10:13], v[176:179], v[220:223], v[10:13]
	v_mfma_f32_16x16x32_bf16 v[2:5], v[184:187], v[220:223], v[2:5]
	s_setprio 0
	s_barrier
	s_add_u32 s30, s30, 0x100
	s_addc_u32 s31, s31, 0
	s_add_u32 s58, s58, 0x100
	s_addc_u32 s59, s59, 0
	s_cmp_ge_i32 s61, s47
	s_mov_b32 s34, s61
	s_cbranch_scc0 .LBB0_1171

; #define PG8_STAGE(bufoff, gbase, voff) do { _Pragma("unroll") for (int _i = 0; _i < 2; ++_i) \
;         __builtin_amdgcn_global_load_lds((const unsigned*)((const char*)(gbase) + (voff)[_i]), (PG8_LAS unsigned*)(lds + (bufoff) + ldsw + _i * 8192), 16, 0, 0); } while (0)
; #define PG8_LDA(dst, b, h) do { _Pragma("unroll") for (int m = 0; m < 4; ++m) { const bf16x8 f0_ = *(const PG8_LAS bf16x8*)(lds + PG8_SA(b, h) + aoff + m * 2048), f1_ = *(const PG8_LAS bf16x8*)(lds + PG8_SA(b, h) + aoff + m * 2048 + 1024); dst[m].set(f0_, f1_); } } while (0)
; #define PG8_LDB(dst, b, h) do { _Pragma("unroll") for (int n = 0; n < 2; ++n) { const bf16x8 f0_ = *(const PG8_LAS bf16x8*)(lds + PG8_SB(b, h) + boff + n * 2048), f1_ = *(const PG8_LAS bf16x8*)(lds + PG8_SB(b, h) + boff + n * 2048 + 1024); dst[n].set(f0_, f1_); } } while (0)
; #define PG8_WAIT_V(n) asm volatile("s_waitcnt vmcnt(" #n ")" ::: "memory")
; #define PG8_WAIT_L(n) asm volatile("s_waitcnt lgkmcnt(" #n ")" ::: "memory")
; #define PG8_BAR __builtin_amdgcn_s_barrier()
; #define PG8_SCHED __builtin_amdgcn_sched_barrier(0)
; template <class Epi, class Sched, bool ALIGN_EPI = false, bool SP2 = false>
; __device__ __forceinline__ void gemm_phase(PG8_LAS unsigned char* lds, const Gemm g, const Sched& S, const Epi& E) {
;     ...
;             const bool last = (t == nt - 2);
;             const char* a1 = cA + (size_t)(t + 1) * kstep;
;             const char* a2 = last ? nA : cA + (size_t)(t + 2) * kstep; const char* b2 = last ? nB : cB + (size_t)(t + 2) * kstep;
;             const char* a3 = a2 + kstep; const char* b3 = b2 + kstep;
;             if (last && has_next) S.a_ready(nxt);
;             if constexpr (SP2) {
;             PG8_LDB(B0, 0, 0); PG8_LDB(B1, 0, 1); PG8_SCHED; PG8_LDA(At, 0, 0); PG8_STAGE(PG8_SA(1, 1), a1 + hstep, voffA);
;             PG8_WAIT_V(8); PG8_WAIT_L(0); PG8_BAR; PG8_MMA(0, 0, At, B0); PG8_MMA(0, 1, At, B1); PG8_BAR; PG8_SCHED;
;             PG8_LDA(At, 0, 1); PG8_STAGE(PG8_SB(0, 0), b2, voffB); PG8_STAGE(PG8_SB(0, 1), b2 + hstepB, voffB); PG8_STAGE(PG8_SA(0, 0), a2, voffA);
;             PG8_WAIT_V(8); PG8_WAIT_L(0); PG8_BAR; PG8_MMA(1, 0, At, B0); PG8_MMA(1, 1, At, B1); PG8_BAR; PG8_SCHED;
.LBB0_1592:
	ds_read_b128 v[156:159], v152
	ds_read_b128 v[160:163], v152 offset:1024
	ds_read_b128 v[164:167], v152 offset:2048
	ds_read_b128 v[168:171], v152 offset:3072
	ds_read_b128 v[172:175], v153
	ds_read_b128 v[176:179], v153 offset:1024
	ds_read_b128 v[180:183], v153 offset:2048
	ds_read_b128 v[184:187], v153 offset:3072
	s_add_i32 s61, s34, 2
	s_add_u32 s0, s30, 0x80
	s_addc_u32 s1, s31, 0
	s_cmp_eq_u32 s49, s34
	s_cselect_b32 s34, s6, s0
	s_cselect_b32 s35, s7, s1
	s_cselect_b32 s1, s29, s59
	s_cselect_b32 s0, s28, s58
	v_lshl_add_u64 v[148:149], s[30:31], 0, v[140:141]
	s_add_i32 m0, s40, 0xc000
	ds_read_b128 v[188:191], v154
	ds_read_b128 v[192:195], v154 offset:1024
	ds_read_b128 v[196:199], v154 offset:2048
	ds_read_b128 v[200:203], v154 offset:3072
	ds_read_b128 v[204:207], v154 offset:4096
	ds_read_b128 v[212:215], v154 offset:5120
	ds_read_b128 v[216:219], v154 offset:6144
	ds_read_b128 v[220:223], v154 offset:7168
	global_load_lds_dwordx4 v[148:149], off
	v_lshl_add_u64 v[148:149], s[30:31], 0, v[142:143]
	s_add_i32 m0, s40, 0xe000
	s_nop 0
	global_load_lds_dwordx4 v[148:149], off
	s_waitcnt vmcnt(8)
	s_waitcnt lgkmcnt(0)
	s_barrier
	s_setprio 1
	s_waitcnt lgkmcnt(0)
	v_mfma_f32_16x16x32_bf16 v[126:129], v[156:159], v[188:191], v[126:129]
	v_mfma_f32_16x16x32_bf16 v[122:125], v[164:167], v[188:191], v[122:125]
	v_mfma_f32_16x16x32_bf16 v[110:113], v[156:159], v[196:199], v[110:113]
	v_mfma_f32_16x16x32_bf16 v[106:109], v[164:167], v[196:199], v[106:109]
	v_mfma_f32_16x16x32_bf16 v[94:97], v[156:159], v[204:207], v[94:97]
	v_mfma_f32_16x16x32_bf16 v[90:93], v[164:167], v[204:207], v[90:93]
	v_mfma_f32_16x16x32_bf16 v[78:81], v[156:159], v[216:219], v[78:81]
	v_mfma_f32_16x16x32_bf16 v[74:77], v[164:167], v[216:219], v[74:77]
	v_mfma_f32_16x16x32_bf16 v[126:129], v[160:163], v[192:195], v[126:129]
	v_mfma_f32_16x16x32_bf16 v[122:125], v[168:171], v[192:195], v[122:125]
	v_mfma_f32_16x16x32_bf16 v[110:113], v[160:163], v[200:203], v[110:113]
	v_mfma_f32_16x16x32_bf16 v[106:109], v[168:171], v[200:203], v[106:109]
	v_mfma_f32_16x16x32_bf16 v[94:97], v[160:163], v[212:215], v[94:97]
	v_mfma_f32_16x16x32_bf16 v[90:93], v[168:171], v[212:215], v[90:93]
	v_mfma_f32_16x16x32_bf16 v[78:81], v[160:163], v[220:223], v[78:81]
	v_mfma_f32_16x16x32_bf16 v[74:77], v[168:171], v[220:223], v[74:77]
	s_setprio 0
	s_setprio 1
	v_mfma_f32_16x16x32_bf16 v[118:121], v[172:175], v[188:191], v[118:121]
	v_mfma_f32_16x16x32_bf16 v[114:117], v[180:183], v[188:191], v[114:117]
	v_mfma_f32_16x16x32_bf16 v[102:105], v[172:175], v[196:199], v[102:105]
	v_mfma_f32_16x16x32_bf16 v[98:101], v[180:183], v[196:199], v[98:101]
	v_mfma_f32_16x16x32_bf16 v[86:89], v[172:175], v[204:207], v[86:89]
	v_mfma_f32_16x16x32_bf16 v[82:85], v[180:183], v[204:207], v[82:85]
	v_mfma_f32_16x16x32_bf16 v[70:73], v[172:175], v[216:219], v[70:73]
	v_mfma_f32_16x16x32_bf16 v[66:69], v[180:183], v[216:219], v[66:69]
	v_mfma_f32_16x16x32_bf16 v[118:121], v[176:179], v[192:195], v[118:121]
	v_mfma_f32_16x16x32_bf16 v[114:117], v[184:187], v[192:195], v[114:117]
	v_mfma_f32_16x16x32_bf16 v[102:105], v[176:179], v[200:203], v[102:105]
	v_mfma_f32_16x16x32_bf16 v[98:101], v[184:187], v[200:203], v[98:101]
	v_mfma_f32_16x16x32_bf16 v[86:89], v[176:179], v[212:215], v[86:89]
	v_mfma_f32_16x16x32_bf16 v[82:85], v[184:187], v[212:215], v[82:85]
	v_mfma_f32_16x16x32_bf16 v[70:73], v[176:179], v[220:223], v[70:73]
	v_mfma_f32_16x16x32_bf16 v[66:69], v[184:187], v[220:223], v[66:69]
	s_setprio 0
	s_barrier
	s_add_i32 s33, s52, s39
	v_lshl_add_u64 v[148:149], s[0:1], 0, v[132:133]
	s_mov_b32 m0, s33
	ds_read_b128 v[188:191], v154 offset:16384
	ds_read_b128 v[192:195], v154 offset:17408
	ds_read_b128 v[196:199], v154 offset:18432
	ds_read_b128 v[200:203], v154 offset:19456
	ds_read_b128 v[204:207], v154 offset:20480
	ds_read_b128 v[212:215], v154 offset:21504
	ds_read_b128 v[216:219], v154 offset:22528
	ds_read_b128 v[220:223], v154 offset:23552
	global_load_lds_dwordx4 v[148:149], off
	s_add_i32 m0, s33, 0x2000
	v_lshl_add_u64 v[208:209], s[0:1], 0, v[136:137]
	s_add_u32 s0, s0, s14
	s_addc_u32 s1, s1, s15
	s_add_i32 s33, s53, s39
	global_load_lds_dwordx4 v[208:209], off
	v_lshl_add_u64 v[224:225], s[0:1], 0, v[132:133]
	s_mov_b32 m0, s33
	v_lshl_add_u64 v[226:227], s[0:1], 0, v[136:137]
	global_load_lds_dwordx4 v[224:225], off
	s_add_i32 m0, s33, 0x2000
	v_lshl_add_u64 v[228:229], s[34:35], 0, v[130:131]
	global_load_lds_dwordx4 v[226:227], off
	v_lshl_add_u64 v[230:231], s[34:35], 0, v[134:135]
	s_waitcnt vmcnt(6)
	s_waitcnt lgkmcnt(0)
	s_barrier
; #define PG8_STAGE(bufoff, gbase, voff) do { _Pragma("unroll") for (int _i = 0; _i < 2; ++_i) \
;         __builtin_amdgcn_global_load_lds((const unsigned*)((const char*)(gbase) + (voff)[_i]), (PG8_LAS unsigned*)(lds + (bufoff) + ldsw + _i * 8192), 16, 0, 0); } while (0)
; #define PG8_LDA(dst, b, h) do { _Pragma("unroll") for (int m = 0; m < 4; ++m) { const bf16x8 f0_ = *(const PG8_LAS bf16x8*)(lds + PG8_SA(b, h) + aoff + m * 2048), f1_ = *(const PG8_LAS bf16x8*)(lds + PG8_SA(b, h) + aoff + m * 2048 + 1024); dst[m].set(f0_, f1_); } } while (0)
; #define PG8_LDB(dst, b, h) do { _Pragma("unroll") for (int n = 0; n < 2; ++n) { const bf16x8 f0_ = *(const PG8_LAS bf16x8*)(lds + PG8_SB(b, h) + boff + n * 2048), f1_ = *(const PG8_LAS bf16x8*)(lds + PG8_SB(b, h) + boff + n * 2048 + 1024); dst[n].set(f0_, f1_); } } while (0)
; #define PG8_WAIT_V(n) asm volatile("s_waitcnt vmcnt(" #n ")" ::: "memory")
; #define PG8_WAIT_L(n) asm volatile("s_waitcnt lgkmcnt(" #n ")" ::: "memory")
; #define PG8_BAR __builtin_amdgcn_s_barrier()
; #define PG8_SCHED __builtin_amdgcn_sched_barrier(0)
; template <class Epi, class Sched, bool ALIGN_EPI = false, bool SP2 = false>
; __device__ __forceinline__ void gemm_phase(PG8_LAS unsigned char* lds, const Gemm g, const Sched& S, const Epi& E) {
;     ...
;             PG8_WAIT_V(8); PG8_WAIT_L(0); PG8_BAR; PG8_MMA(1, 0, At, B0); PG8_MMA(1, 1, At, B1); PG8_BAR; PG8_SCHED;
;             PG8_LDB(B0, 1, 0); PG8_LDB(B1, 1, 1); PG8_SCHED; PG8_LDA(At, 1, 0); PG8_STAGE(PG8_SA(0, 1), a2 + hstep, voffA);
;             PG8_WAIT_V(8); PG8_WAIT_L(0); PG8_BAR; PG8_MMA(0, 0, At, B0); PG8_MMA(0, 1, At, B1); PG8_BAR; PG8_SCHED;
	s_setprio 1
	s_waitcnt lgkmcnt(0)
	v_mfma_f32_16x16x32_bf16 v[62:65], v[156:159], v[188:191], v[62:65]
	v_mfma_f32_16x16x32_bf16 v[58:61], v[164:167], v[188:191], v[58:61]
	v_mfma_f32_16x16x32_bf16 v[46:49], v[156:159], v[196:199], v[46:49]
	v_mfma_f32_16x16x32_bf16 v[42:45], v[164:167], v[196:199], v[42:45]
	v_mfma_f32_16x16x32_bf16 v[30:33], v[156:159], v[204:207], v[30:33]
	v_mfma_f32_16x16x32_bf16 v[26:29], v[164:167], v[204:207], v[26:29]
	v_mfma_f32_16x16x32_bf16 v[14:17], v[156:159], v[216:219], v[14:17]
	v_mfma_f32_16x16x32_bf16 v[6:9], v[164:167], v[216:219], v[6:9]
	v_mfma_f32_16x16x32_bf16 v[62:65], v[160:163], v[192:195], v[62:65]
	v_mfma_f32_16x16x32_bf16 v[58:61], v[168:171], v[192:195], v[58:61]
	v_mfma_f32_16x16x32_bf16 v[46:49], v[160:163], v[200:203], v[46:49]
	v_mfma_f32_16x16x32_bf16 v[42:45], v[168:171], v[200:203], v[42:45]
	v_mfma_f32_16x16x32_bf16 v[30:33], v[160:163], v[212:215], v[30:33]
	v_mfma_f32_16x16x32_bf16 v[26:29], v[168:171], v[212:215], v[26:29]
	v_mfma_f32_16x16x32_bf16 v[14:17], v[160:163], v[220:223], v[14:17]
	v_mfma_f32_16x16x32_bf16 v[6:9], v[168:171], v[220:223], v[6:9]
	s_setprio 0
	s_setprio 1
	v_mfma_f32_16x16x32_bf16 v[54:57], v[172:175], v[188:191], v[54:57]
	v_mfma_f32_16x16x32_bf16 v[50:53], v[180:183], v[188:191], v[50:53]
	v_mfma_f32_16x16x32_bf16 v[38:41], v[172:175], v[196:199], v[38:41]
	v_mfma_f32_16x16x32_bf16 v[34:37], v[180:183], v[196:199], v[34:37]
	v_mfma_f32_16x16x32_bf16 v[22:25], v[172:175], v[204:207], v[22:25]
	v_mfma_f32_16x16x32_bf16 v[18:21], v[180:183], v[204:207], v[18:21]
	v_mfma_f32_16x16x32_bf16 v[10:13], v[172:175], v[216:219], v[10:13]
	v_mfma_f32_16x16x32_bf16 v[2:5], v[180:183], v[216:219], v[2:5]
	v_mfma_f32_16x16x32_bf16 v[54:57], v[176:179], v[192:195], v[54:57]
	v_mfma_f32_16x16x32_bf16 v[50:53], v[184:187], v[192:195], v[50:53]
	v_mfma_f32_16x16x32_bf16 v[38:41], v[176:179], v[200:203], v[38:41]
	v_mfma_f32_16x16x32_bf16 v[34:37], v[184:187], v[200:203], v[34:37]
	v_mfma_f32_16x16x32_bf16 v[22:25], v[176:179], v[212:215], v[22:25]
	v_mfma_f32_16x16x32_bf16 v[18:21], v[184:187], v[212:215], v[18:21]
	v_mfma_f32_16x16x32_bf16 v[10:13], v[176:179], v[220:223], v[10:13]
	v_mfma_f32_16x16x32_bf16 v[2:5], v[184:187], v[220:223], v[2:5]
	s_setprio 0
	s_barrier
	s_add_i32 s33, 0, 0x18000
	s_add_i32 s63, 0, 0x1c000
	v_add_u32_e32 v168, s33, v1
	v_add_u32_e32 v184, s63, v1
	ds_read_b128 v[156:159], v168
	ds_read_b128 v[160:163], v168 offset:1024
	ds_read_b128 v[164:167], v168 offset:2048
	ds_read_b128 v[168:171], v168 offset:3072
	ds_read_b128 v[172:175], v184
	ds_read_b128 v[176:179], v184 offset:1024
	ds_read_b128 v[180:183], v184 offset:2048
	ds_read_b128 v[184:187], v184 offset:3072
	s_add_u32 s0, s34, s12
	s_addc_u32 s1, s35, s13
	s_mov_b32 m0, s42
	v_lshl_add_u64 v[232:233], s[0:1], 0, v[130:131]
	ds_read_b128 v[188:191], v154 offset:32768
	ds_read_b128 v[192:195], v154 offset:33792
	ds_read_b128 v[196:199], v154 offset:34816
	ds_read_b128 v[200:203], v154 offset:35840
	ds_read_b128 v[204:207], v154 offset:36864
	ds_read_b128 v[212:215], v154 offset:37888
	ds_read_b128 v[216:219], v154 offset:38912
	ds_read_b128 v[220:223], v154 offset:39936
	global_load_lds_dwordx4 v[232:233], off
	v_lshl_add_u64 v[232:233], s[0:1], 0, v[134:135]
	s_mov_b32 m0, s43
	s_nop 0
	global_load_lds_dwordx4 v[232:233], off
	s_mov_b32 m0, s40
	s_nop 0
	global_load_lds_dwordx4 v[228:229], off
	s_mov_b32 m0, s41
	s_nop 0
	global_load_lds_dwordx4 v[230:231], off
	s_waitcnt vmcnt(8)
	s_waitcnt lgkmcnt(0)
	s_barrier
	s_setprio 1
	s_waitcnt lgkmcnt(0)
	v_mfma_f32_16x16x32_bf16 v[126:129], v[156:159], v[188:191], v[126:129]
	v_mfma_f32_16x16x32_bf16 v[122:125], v[164:167], v[188:191], v[122:125]
	v_mfma_f32_16x16x32_bf16 v[110:113], v[156:159], v[196:199], v[110:113]
	v_mfma_f32_16x16x32_bf16 v[106:109], v[164:167], v[196:199], v[106:109]
	v_mfma_f32_16x16x32_bf16 v[94:97], v[156:159], v[204:207], v[94:97]
	v_mfma_f32_16x16x32_bf16 v[90:93], v[164:167], v[204:207], v[90:93]
	v_mfma_f32_16x16x32_bf16 v[78:81], v[156:159], v[216:219], v[78:81]
	v_mfma_f32_16x16x32_bf16 v[74:77], v[164:167], v[216:219], v[74:77]
	v_mfma_f32_16x16x32_bf16 v[126:129], v[160:163], v[192:195], v[126:129]
	v_mfma_f32_16x16x32_bf16 v[122:125], v[168:171], v[192:195], v[122:125]
	v_mfma_f32_16x16x32_bf16 v[110:113], v[160:163], v[200:203], v[110:113]
	v_mfma_f32_16x16x32_bf16 v[106:109], v[168:171], v[200:203], v[106:109]
	v_mfma_f32_16x16x32_bf16 v[94:97], v[160:163], v[212:215], v[94:97]
	v_mfma_f32_16x16x32_bf16 v[90:93], v[168:171], v[212:215], v[90:93]
	v_mfma_f32_16x16x32_bf16 v[78:81], v[160:163], v[220:223], v[78:81]
	v_mfma_f32_16x16x32_bf16 v[74:77], v[168:171], v[220:223], v[74:77]
	s_setprio 0
	s_setprio 1
	v_mfma_f32_16x16x32_bf16 v[118:121], v[172:175], v[188:191], v[118:121]
	v_mfma_f32_16x16x32_bf16 v[114:117], v[180:183], v[188:191], v[114:117]
	v_mfma_f32_16x16x32_bf16 v[102:105], v[172:175], v[196:199], v[102:105]
	v_mfma_f32_16x16x32_bf16 v[98:101], v[180:183], v[196:199], v[98:101]
	v_mfma_f32_16x16x32_bf16 v[86:89], v[172:175], v[204:207], v[86:89]
	v_mfma_f32_16x16x32_bf16 v[82:85], v[180:183], v[204:207], v[82:85]
	v_mfma_f32_16x16x32_bf16 v[70:73], v[172:175], v[216:219], v[70:73]
	v_mfma_f32_16x16x32_bf16 v[66:69], v[180:183], v[216:219], v[66:69]
	v_mfma_f32_16x16x32_bf16 v[118:121], v[176:179], v[192:195], v[118:121]
	v_mfma_f32_16x16x32_bf16 v[114:117], v[184:187], v[192:195], v[114:117]
	v_mfma_f32_16x16x32_bf16 v[102:105], v[176:179], v[200:203], v[102:105]
	v_mfma_f32_16x16x32_bf16 v[98:101], v[184:187], v[200:203], v[98:101]
	v_mfma_f32_16x16x32_bf16 v[86:89], v[176:179], v[212:215], v[86:89]
	v_mfma_f32_16x16x32_bf16 v[82:85], v[184:187], v[212:215], v[82:85]
	v_mfma_f32_16x16x32_bf16 v[70:73], v[176:179], v[220:223], v[70:73]
	v_mfma_f32_16x16x32_bf16 v[66:69], v[184:187], v[220:223], v[66:69]
	s_setprio 0
	s_barrier
; #define PG8_STAGE(bufoff, gbase, voff) do { _Pragma("unroll") for (int _i = 0; _i < 2; ++_i) \
;         __builtin_amdgcn_global_load_lds((const unsigned*)((const char*)(gbase) + (voff)[_i]), (PG8_LAS unsigned*)(lds + (bufoff) + ldsw + _i * 8192), 16, 0, 0); } while (0)
; #define PG8_LDA(dst, b, h) do { _Pragma("unroll") for (int m = 0; m < 4; ++m) { const bf16x8 f0_ = *(const PG8_LAS bf16x8*)(lds + PG8_SA(b, h) + aoff + m * 2048), f1_ = *(const PG8_LAS bf16x8*)(lds + PG8_SA(b, h) + aoff + m * 2048 + 1024); dst[m].set(f0_, f1_); } } while (0)
; #define PG8_WAIT_V(n) asm volatile("s_waitcnt vmcnt(" #n ")" ::: "memory")
; #define PG8_WAIT_L(n) asm volatile("s_waitcnt lgkmcnt(" #n ")" ::: "memory")
; #define PG8_BAR __builtin_amdgcn_s_barrier()
; #define PG8_SCHED __builtin_amdgcn_sched_barrier(0)
; template <class Epi, class Sched, bool ALIGN_EPI = false, bool SP2 = false>
; __device__ __forceinline__ void gemm_phase(PG8_LAS unsigned char* lds, const Gemm g, const Sched& S, const Epi& E) {
;     ...
;             PG8_LDA(At, 1, 1); PG8_STAGE(PG8_SB(1, 0), b3, voffB); PG8_STAGE(PG8_SB(1, 1), b3 + hstepB, voffB); PG8_STAGE(PG8_SA(1, 0), a3, voffA);
;             PG8_WAIT_V(8); PG8_WAIT_L(0); PG8_BAR; PG8_MMA(1, 0, At, B0); PG8_MMA(1, 1, At, B1); PG8_BAR; PG8_SCHED;
	s_add_i32 s0, s33, s39
	v_lshl_add_u64 v[148:149], v[148:149], 0, s[22:23]
	s_mov_b32 m0, s0
	ds_read_b128 v[188:191], v154 offset:49152
	ds_read_b128 v[192:195], v154 offset:50176
	ds_read_b128 v[196:199], v154 offset:51200
	ds_read_b128 v[200:203], v154 offset:52224
	ds_read_b128 v[204:207], v154 offset:53248
	ds_read_b128 v[212:215], v154 offset:54272
	ds_read_b128 v[216:219], v154 offset:55296
	ds_read_b128 v[220:223], v154 offset:56320
	global_load_lds_dwordx4 v[148:149], off
	v_lshl_add_u64 v[148:149], v[208:209], 0, s[22:23]
	s_add_i32 m0, s0, 0x2000
	s_add_i32 s0, s63, s39
	global_load_lds_dwordx4 v[148:149], off
	v_lshl_add_u64 v[148:149], v[224:225], 0, s[22:23]
	s_mov_b32 m0, s0
	s_nop 0
	global_load_lds_dwordx4 v[148:149], off
	v_lshl_add_u64 v[148:149], v[226:227], 0, s[22:23]
	s_add_i32 m0, s0, 0x2000
	s_nop 0
	global_load_lds_dwordx4 v[148:149], off
	v_lshl_add_u64 v[148:149], v[228:229], 0, s[22:23]
	s_mov_b32 m0, s46
	s_nop 0
	global_load_lds_dwordx4 v[148:149], off
	v_lshl_add_u64 v[148:149], v[230:231], 0, s[22:23]
	s_mov_b32 m0, s47
	s_nop 0
	global_load_lds_dwordx4 v[148:149], off
	s_waitcnt vmcnt(6)
	s_waitcnt lgkmcnt(0)
	s_barrier
	s_setprio 1
	s_waitcnt lgkmcnt(0)
	v_mfma_f32_16x16x32_bf16 v[62:65], v[156:159], v[188:191], v[62:65]
	v_mfma_f32_16x16x32_bf16 v[58:61], v[164:167], v[188:191], v[58:61]
	v_mfma_f32_16x16x32_bf16 v[46:49], v[156:159], v[196:199], v[46:49]
	v_mfma_f32_16x16x32_bf16 v[42:45], v[164:167], v[196:199], v[42:45]
	v_mfma_f32_16x16x32_bf16 v[30:33], v[156:159], v[204:207], v[30:33]
	v_mfma_f32_16x16x32_bf16 v[26:29], v[164:167], v[204:207], v[26:29]
	v_mfma_f32_16x16x32_bf16 v[14:17], v[156:159], v[216:219], v[14:17]
	v_mfma_f32_16x16x32_bf16 v[6:9], v[164:167], v[216:219], v[6:9]
	v_mfma_f32_16x16x32_bf16 v[62:65], v[160:163], v[192:195], v[62:65]
	v_mfma_f32_16x16x32_bf16 v[58:61], v[168:171], v[192:195], v[58:61]
	v_mfma_f32_16x16x32_bf16 v[46:49], v[160:163], v[200:203], v[46:49]
	v_mfma_f32_16x16x32_bf16 v[42:45], v[168:171], v[200:203], v[42:45]
	v_mfma_f32_16x16x32_bf16 v[30:33], v[160:163], v[212:215], v[30:33]
	v_mfma_f32_16x16x32_bf16 v[26:29], v[168:171], v[212:215], v[26:29]
	v_mfma_f32_16x16x32_bf16 v[14:17], v[160:163], v[220:223], v[14:17]
	v_mfma_f32_16x16x32_bf16 v[6:9], v[168:171], v[220:223], v[6:9]
	s_setprio 0
	s_setprio 1
	v_mfma_f32_16x16x32_bf16 v[54:57], v[172:175], v[188:191], v[54:57]
	v_mfma_f32_16x16x32_bf16 v[50:53], v[180:183], v[188:191], v[50:53]
	v_mfma_f32_16x16x32_bf16 v[38:41], v[172:175], v[196:199], v[38:41]
	v_mfma_f32_16x16x32_bf16 v[34:37], v[180:183], v[196:199], v[34:37]
	v_mfma_f32_16x16x32_bf16 v[22:25], v[172:175], v[204:207], v[22:25]
	v_mfma_f32_16x16x32_bf16 v[18:21], v[180:183], v[204:207], v[18:21]
	v_mfma_f32_16x16x32_bf16 v[10:13], v[172:175], v[216:219], v[10:13]
	v_mfma_f32_16x16x32_bf16 v[2:5], v[180:183], v[216:219], v[2:5]
	v_mfma_f32_16x16x32_bf16 v[54:57], v[176:179], v[192:195], v[54:57]
	v_mfma_f32_16x16x32_bf16 v[50:53], v[184:187], v[192:195], v[50:53]
	v_mfma_f32_16x16x32_bf16 v[38:41], v[176:179], v[200:203], v[38:41]
	v_mfma_f32_16x16x32_bf16 v[34:37], v[184:187], v[200:203], v[34:37]
	v_mfma_f32_16x16x32_bf16 v[22:25], v[176:179], v[212:215], v[22:25]
	v_mfma_f32_16x16x32_bf16 v[18:21], v[184:187], v[212:215], v[18:21]
	v_mfma_f32_16x16x32_bf16 v[10:13], v[176:179], v[220:223], v[10:13]
	v_mfma_f32_16x16x32_bf16 v[2:5], v[184:187], v[220:223], v[2:5]
	s_setprio 0
	s_barrier
	s_add_u32 s30, s30, 0x100
	s_addc_u32 s31, s31, 0
	s_add_u32 s58, s58, 0x100
	s_addc_u32 s59, s59, 0
	s_cmp_ge_i32 s61, s48
	s_mov_b32 s34, s61
	s_cbranch_scc0 .LBB0_1592

; #define PG8_STAGE(bufoff, gbase, voff) do { _Pragma("unroll") for (int _i = 0; _i < 2; ++_i) \
;         __builtin_amdgcn_global_load_lds((const unsigned*)((const char*)(gbase) + (voff)[_i]), (PG8_LAS unsigned*)(lds + (bufoff) + ldsw + _i * 8192), 16, 0, 0); } while (0)
; #define PG8_LDA(dst, b, h) do { _Pragma("unroll") for (int m = 0; m < 4; ++m) { const bf16x8 f0_ = *(const PG8_LAS bf16x8*)(lds + PG8_SA(b, h) + aoff + m * 2048), f1_ = *(const PG8_LAS bf16x8*)(lds + PG8_SA(b, h) + aoff + m * 2048 + 1024); dst[m].set(f0_, f1_); } } while (0)
; #define PG8_LDB(dst, b, h) do { _Pragma("unroll") for (int n = 0; n < 2; ++n) { const bf16x8 f0_ = *(const PG8_LAS bf16x8*)(lds + PG8_SB(b, h) + boff + n * 2048), f1_ = *(const PG8_LAS bf16x8*)(lds + PG8_SB(b, h) + boff + n * 2048 + 1024); dst[n].set(f0_, f1_); } } while (0)
; #define PG8_WAIT_V(n) asm volatile("s_waitcnt vmcnt(" #n ")" ::: "memory")
; #define PG8_WAIT_L(n) asm volatile("s_waitcnt lgkmcnt(" #n ")" ::: "memory")
; #define PG8_BAR __builtin_amdgcn_s_barrier()
; #define PG8_SCHED __builtin_amdgcn_sched_barrier(0)
; template <class Epi, class Sched, bool ALIGN_EPI = false, bool SP2 = false>
; __device__ __forceinline__ void gemm_phase(PG8_LAS unsigned char* lds, const Gemm g, const Sched& S, const Epi& E) {
;     ...
;             const bool last = (t == nt - 2);
;             const char* a1 = cA + (size_t)(t + 1) * kstep;
;             const char* a2 = last ? nA : cA + (size_t)(t + 2) * kstep; const char* b2 = last ? nB : cB + (size_t)(t + 2) * kstep;
;             const char* a3 = a2 + kstep; const char* b3 = b2 + kstep;
;             if (last && has_next) S.a_ready(nxt);
;             if constexpr (SP2) {
;             PG8_LDB(B0, 0, 0); PG8_LDB(B1, 0, 1); PG8_SCHED; PG8_LDA(At, 0, 0); PG8_STAGE(PG8_SA(1, 1), a1 + hstep, voffA);
;             PG8_WAIT_V(8); PG8_WAIT_L(0); PG8_BAR; PG8_MMA(0, 0, At, B0); PG8_MMA(0, 1, At, B1); PG8_BAR; PG8_SCHED;
;             PG8_LDA(At, 0, 1); PG8_STAGE(PG8_SB(0, 0), b2, voffB); PG8_STAGE(PG8_SB(0, 1), b2 + hstepB, voffB); PG8_STAGE(PG8_SA(0, 0), a2, voffA);
;             PG8_WAIT_V(8); PG8_WAIT_L(0); PG8_BAR; PG8_MMA(1, 0, At, B0); PG8_MMA(1, 1, At, B1); PG8_BAR; PG8_SCHED;
.LBB0_1625:
	ds_read_b128 v[18:21], v197
	ds_read_b128 v[22:25], v197 offset:1024
	ds_read_b128 v[26:29], v197 offset:2048
	ds_read_b128 v[30:33], v197 offset:3072
	ds_read_b128 v[2:5], v198
	ds_read_b128 v[6:9], v198 offset:1024
	ds_read_b128 v[10:13], v198 offset:2048
	ds_read_b128 v[14:17], v198 offset:3072
	s_add_i32 s82, s48, 2
	s_add_u32 s0, s46, 0x80
	s_addc_u32 s1, s47, 0
	s_cmp_eq_u32 s66, s48
	s_cselect_b32 s48, s2, s0
	s_cselect_b32 s49, s3, s1
	s_cselect_b32 s51, s45, s81
	s_cselect_b32 s50, s44, s80
	v_lshl_add_u64 v[192:193], s[46:47], 0, v[176:177]
	s_add_i32 m0, s10, 0xc000
	ds_read_b128 v[184:187], v199
	ds_read_b128 v[188:191], v199 offset:1024
	ds_read_b128 v[212:215], v199 offset:2048
	ds_read_b128 v[216:219], v199 offset:3072
	ds_read_b128 v[220:223], v199 offset:4096
	ds_read_b128 v[224:227], v199 offset:5120
	ds_read_b128 v[228:231], v199 offset:6144
	ds_read_b128 v[232:235], v199 offset:7168
	global_load_lds_dwordx4 v[192:193], off
	v_lshl_add_u64 v[192:193], s[46:47], 0, v[178:179]
	s_add_i32 m0, s10, 0xe000
	s_nop 0
	global_load_lds_dwordx4 v[192:193], off
	s_waitcnt vmcnt(8)
	s_waitcnt lgkmcnt(0)
	s_barrier
	s_setprio 1
	s_waitcnt lgkmcnt(0)
	v_mfma_scale_f32_16x16x128_f8f6f4 v[158:161], v[18:25], v[184:191], v[158:161], v200, v201 op_sel_hi:[0,0,0]
	v_mfma_scale_f32_16x16x128_f8f6f4 v[154:157], v[26:33], v[184:191], v[154:157], v200, v201 op_sel_hi:[0,0,0]
	v_mfma_scale_f32_16x16x128_f8f6f4 v[142:145], v[18:25], v[212:219], v[142:145], v200, v201 op_sel_hi:[0,0,0]
	v_mfma_scale_f32_16x16x128_f8f6f4 v[138:141], v[26:33], v[212:219], v[138:141], v200, v201 op_sel_hi:[0,0,0]
	v_mfma_scale_f32_16x16x128_f8f6f4 v[126:129], v[18:25], v[220:227], v[126:129], v200, v201 op_sel_hi:[0,0,0]
	v_mfma_scale_f32_16x16x128_f8f6f4 v[122:125], v[26:33], v[220:227], v[122:125], v200, v201 op_sel_hi:[0,0,0]
	v_mfma_scale_f32_16x16x128_f8f6f4 v[110:113], v[18:25], v[228:235], v[110:113], v200, v201 op_sel_hi:[0,0,0]
	v_mfma_scale_f32_16x16x128_f8f6f4 v[106:109], v[26:33], v[228:235], v[106:109], v200, v201 op_sel_hi:[0,0,0]
	s_setprio 0
	s_setprio 1
	v_mfma_scale_f32_16x16x128_f8f6f4 v[150:153], v[2:9], v[184:191], v[150:153], v200, v201 op_sel_hi:[0,0,0]
	v_mfma_scale_f32_16x16x128_f8f6f4 v[146:149], v[10:17], v[184:191], v[146:149], v200, v201 op_sel_hi:[0,0,0]
	v_mfma_scale_f32_16x16x128_f8f6f4 v[134:137], v[2:9], v[212:219], v[134:137], v200, v201 op_sel_hi:[0,0,0]
	v_mfma_scale_f32_16x16x128_f8f6f4 v[130:133], v[10:17], v[212:219], v[130:133], v200, v201 op_sel_hi:[0,0,0]
	v_mfma_scale_f32_16x16x128_f8f6f4 v[118:121], v[2:9], v[220:227], v[118:121], v200, v201 op_sel_hi:[0,0,0]
	v_mfma_scale_f32_16x16x128_f8f6f4 v[114:117], v[10:17], v[220:227], v[114:117], v200, v201 op_sel_hi:[0,0,0]
	v_mfma_scale_f32_16x16x128_f8f6f4 v[102:105], v[2:9], v[228:235], v[102:105], v200, v201 op_sel_hi:[0,0,0]
	v_mfma_scale_f32_16x16x128_f8f6f4 v[98:101], v[10:17], v[228:235], v[98:101], v200, v201 op_sel_hi:[0,0,0]
	s_setprio 0
	s_barrier
	s_add_i32 s0, s73, s9
	v_lshl_add_u64 v[184:185], s[50:51], 0, v[164:165]
	s_mov_b32 m0, s0
	ds_read_b128 v[212:215], v199 offset:16384
	ds_read_b128 v[216:219], v199 offset:17408
	ds_read_b128 v[220:223], v199 offset:18432
	ds_read_b128 v[224:227], v199 offset:19456
	ds_read_b128 v[228:231], v199 offset:20480
	ds_read_b128 v[232:235], v199 offset:21504
	ds_read_b128 v[236:239], v199 offset:22528
	ds_read_b128 v[240:243], v199 offset:23552
	global_load_lds_dwordx4 v[184:185], off
	s_add_i32 m0, s0, 0x2000
	s_add_u32 s0, s50, s14
	v_lshl_add_u64 v[186:187], s[50:51], 0, v[168:169]
	s_addc_u32 s1, s51, s15
	s_add_i32 s33, s74, s9
	global_load_lds_dwordx4 v[186:187], off
	v_lshl_add_u64 v[188:189], s[0:1], 0, v[164:165]
	s_mov_b32 m0, s33
	v_lshl_add_u64 v[190:191], s[0:1], 0, v[168:169]
	global_load_lds_dwordx4 v[188:189], off
	s_add_i32 m0, s33, 0x2000
	v_lshl_add_u64 v[192:193], s[48:49], 0, v[162:163]
	global_load_lds_dwordx4 v[190:191], off
	v_lshl_add_u64 v[194:195], s[48:49], 0, v[166:167]
	s_waitcnt vmcnt(6)
	s_waitcnt lgkmcnt(0)
	s_barrier
	s_setprio 1
	s_waitcnt lgkmcnt(0)
	v_mfma_scale_f32_16x16x128_f8f6f4 v[94:97], v[18:25], v[212:219], v[94:97], v200, v201 op_sel_hi:[0,0,0]
	v_mfma_scale_f32_16x16x128_f8f6f4 v[90:93], v[26:33], v[212:219], v[90:93], v200, v201 op_sel_hi:[0,0,0]
	v_mfma_scale_f32_16x16x128_f8f6f4 v[78:81], v[18:25], v[220:227], v[78:81], v200, v201 op_sel_hi:[0,0,0]
	v_mfma_scale_f32_16x16x128_f8f6f4 v[74:77], v[26:33], v[220:227], v[74:77], v200, v201 op_sel_hi:[0,0,0]
	v_mfma_scale_f32_16x16x128_f8f6f4 v[62:65], v[18:25], v[228:235], v[62:65], v200, v201 op_sel_hi:[0,0,0]
	v_mfma_scale_f32_16x16x128_f8f6f4 v[58:61], v[26:33], v[228:235], v[58:61], v200, v201 op_sel_hi:[0,0,0]
	v_mfma_scale_f32_16x16x128_f8f6f4 v[46:49], v[18:25], v[236:243], v[46:49], v200, v201 op_sel_hi:[0,0,0]
	v_mfma_scale_f32_16x16x128_f8f6f4 v[42:45], v[26:33], v[236:243], v[42:45], v200, v201 op_sel_hi:[0,0,0]
	s_setprio 0
	s_setprio 1
	v_mfma_scale_f32_16x16x128_f8f6f4 v[86:89], v[2:9], v[212:219], v[86:89], v200, v201 op_sel_hi:[0,0,0]
	v_mfma_scale_f32_16x16x128_f8f6f4 v[82:85], v[10:17], v[212:219], v[82:85], v200, v201 op_sel_hi:[0,0,0]
	v_mfma_scale_f32_16x16x128_f8f6f4 v[70:73], v[2:9], v[220:227], v[70:73], v200, v201 op_sel_hi:[0,0,0]
	v_mfma_scale_f32_16x16x128_f8f6f4 v[66:69], v[10:17], v[220:227], v[66:69], v200, v201 op_sel_hi:[0,0,0]
	v_mfma_scale_f32_16x16x128_f8f6f4 v[54:57], v[2:9], v[228:235], v[54:57], v200, v201 op_sel_hi:[0,0,0]
	v_mfma_scale_f32_16x16x128_f8f6f4 v[50:53], v[10:17], v[228:235], v[50:53], v200, v201 op_sel_hi:[0,0,0]
	v_mfma_scale_f32_16x16x128_f8f6f4 v[38:41], v[2:9], v[236:243], v[38:41], v200, v201 op_sel_hi:[0,0,0]
	v_mfma_scale_f32_16x16x128_f8f6f4 v[34:37], v[10:17], v[236:243], v[34:37], v200, v201 op_sel_hi:[0,0,0]
	s_setprio 0
	s_barrier
; #define PG8_STAGE(bufoff, gbase, voff) do { _Pragma("unroll") for (int _i = 0; _i < 2; ++_i) \
;         __builtin_amdgcn_global_load_lds((const unsigned*)((const char*)(gbase) + (voff)[_i]), (PG8_LAS unsigned*)(lds + (bufoff) + ldsw + _i * 8192), 16, 0, 0); } while (0)
; #define PG8_LDA(dst, b, h) do { _Pragma("unroll") for (int m = 0; m < 4; ++m) { const bf16x8 f0_ = *(const PG8_LAS bf16x8*)(lds + PG8_SA(b, h) + aoff + m * 2048), f1_ = *(const PG8_LAS bf16x8*)(lds + PG8_SA(b, h) + aoff + m * 2048 + 1024); dst[m].set(f0_, f1_); } } while (0)
; #define PG8_LDB(dst, b, h) do { _Pragma("unroll") for (int n = 0; n < 2; ++n) { const bf16x8 f0_ = *(const PG8_LAS bf16x8*)(lds + PG8_SB(b, h) + boff + n * 2048), f1_ = *(const PG8_LAS bf16x8*)(lds + PG8_SB(b, h) + boff + n * 2048 + 1024); dst[n].set(f0_, f1_); } } while (0)
; #define PG8_WAIT_V(n) asm volatile("s_waitcnt vmcnt(" #n ")" ::: "memory")
; #define PG8_WAIT_L(n) asm volatile("s_waitcnt lgkmcnt(" #n ")" ::: "memory")
; #define PG8_BAR __builtin_amdgcn_s_barrier()
; #define PG8_SCHED __builtin_amdgcn_sched_barrier(0)
; template <class Epi, class Sched, bool ALIGN_EPI = false, bool SP2 = false>
; __device__ __forceinline__ void gemm_phase(PG8_LAS unsigned char* lds, const Gemm g, const Sched& S, const Epi& E) {
;     ...
;             PG8_LDB(B0, 1, 0); PG8_LDB(B1, 1, 1); PG8_SCHED; PG8_LDA(At, 1, 0); PG8_STAGE(PG8_SA(0, 1), a2 + hstep, voffA);
;             PG8_WAIT_V(8); PG8_WAIT_L(0); PG8_BAR; PG8_MMA(0, 0, At, B0); PG8_MMA(0, 1, At, B1); PG8_BAR; PG8_SCHED;
;             PG8_LDA(At, 1, 1); PG8_STAGE(PG8_SB(1, 0), b3, voffB); PG8_STAGE(PG8_SB(1, 1), b3 + hstepB, voffB); PG8_STAGE(PG8_SA(1, 0), a3, voffA);
;             PG8_WAIT_V(8); PG8_WAIT_L(0); PG8_BAR; PG8_MMA(1, 0, At, B0); PG8_MMA(1, 1, At, B1); PG8_BAR; PG8_SCHED;
	s_add_i32 s33, 0, 0x18000
	s_add_i32 s50, 0, 0x1c000
	v_add_u32_e32 v14, s33, v173
	v_add_u32_e32 v30, s50, v173
	ds_read_b128 v[2:5], v14
	ds_read_b128 v[6:9], v14 offset:1024
	ds_read_b128 v[10:13], v14 offset:2048
	ds_read_b128 v[14:17], v14 offset:3072
	ds_read_b128 v[18:21], v30
	ds_read_b128 v[22:25], v30 offset:1024
	ds_read_b128 v[26:29], v30 offset:2048
	ds_read_b128 v[30:33], v30 offset:3072
	s_add_u32 s0, s48, s12
	s_addc_u32 s1, s49, s13
	s_mov_b32 m0, s52
	v_lshl_add_u64 v[204:205], s[0:1], 0, v[162:163]
	ds_read_b128 v[212:215], v199 offset:32768
	ds_read_b128 v[216:219], v199 offset:33792
	ds_read_b128 v[220:223], v199 offset:34816
	ds_read_b128 v[224:227], v199 offset:35840
	ds_read_b128 v[228:231], v199 offset:36864
	ds_read_b128 v[232:235], v199 offset:37888
	ds_read_b128 v[236:239], v199 offset:38912
	ds_read_b128 v[240:243], v199 offset:39936
	global_load_lds_dwordx4 v[204:205], off
	v_lshl_add_u64 v[204:205], s[0:1], 0, v[166:167]
	s_mov_b32 m0, s53
	s_nop 0
	global_load_lds_dwordx4 v[204:205], off
	s_mov_b32 m0, s10
	s_nop 0
	global_load_lds_dwordx4 v[192:193], off
	s_mov_b32 m0, s11
	s_nop 0
	global_load_lds_dwordx4 v[194:195], off
	s_waitcnt vmcnt(8)
	s_waitcnt lgkmcnt(0)
	s_barrier
	s_setprio 1
	s_waitcnt lgkmcnt(0)
	v_mfma_scale_f32_16x16x128_f8f6f4 v[158:161], v[2:9], v[212:219], v[158:161], v200, v201 op_sel_hi:[0,0,0]
	v_mfma_scale_f32_16x16x128_f8f6f4 v[154:157], v[10:17], v[212:219], v[154:157], v200, v201 op_sel_hi:[0,0,0]
	v_mfma_scale_f32_16x16x128_f8f6f4 v[142:145], v[2:9], v[220:227], v[142:145], v200, v201 op_sel_hi:[0,0,0]
	v_mfma_scale_f32_16x16x128_f8f6f4 v[138:141], v[10:17], v[220:227], v[138:141], v200, v201 op_sel_hi:[0,0,0]
	v_mfma_scale_f32_16x16x128_f8f6f4 v[126:129], v[2:9], v[228:235], v[126:129], v200, v201 op_sel_hi:[0,0,0]
	v_mfma_scale_f32_16x16x128_f8f6f4 v[122:125], v[10:17], v[228:235], v[122:125], v200, v201 op_sel_hi:[0,0,0]
	v_mfma_scale_f32_16x16x128_f8f6f4 v[110:113], v[2:9], v[236:243], v[110:113], v200, v201 op_sel_hi:[0,0,0]
	v_mfma_scale_f32_16x16x128_f8f6f4 v[106:109], v[10:17], v[236:243], v[106:109], v200, v201 op_sel_hi:[0,0,0]
	s_setprio 0
	s_setprio 1
	v_mfma_scale_f32_16x16x128_f8f6f4 v[150:153], v[18:25], v[212:219], v[150:153], v200, v201 op_sel_hi:[0,0,0]
	v_mfma_scale_f32_16x16x128_f8f6f4 v[146:149], v[26:33], v[212:219], v[146:149], v200, v201 op_sel_hi:[0,0,0]
	v_mfma_scale_f32_16x16x128_f8f6f4 v[134:137], v[18:25], v[220:227], v[134:137], v200, v201 op_sel_hi:[0,0,0]
	v_mfma_scale_f32_16x16x128_f8f6f4 v[130:133], v[26:33], v[220:227], v[130:133], v200, v201 op_sel_hi:[0,0,0]
	v_mfma_scale_f32_16x16x128_f8f6f4 v[118:121], v[18:25], v[228:235], v[118:121], v200, v201 op_sel_hi:[0,0,0]
	v_mfma_scale_f32_16x16x128_f8f6f4 v[114:117], v[26:33], v[228:235], v[114:117], v200, v201 op_sel_hi:[0,0,0]
	v_mfma_scale_f32_16x16x128_f8f6f4 v[102:105], v[18:25], v[236:243], v[102:105], v200, v201 op_sel_hi:[0,0,0]
	v_mfma_scale_f32_16x16x128_f8f6f4 v[98:101], v[26:33], v[236:243], v[98:101], v200, v201 op_sel_hi:[0,0,0]
	s_setprio 0
	s_barrier
	s_add_i32 s0, s33, s9
	v_lshl_add_u64 v[184:185], v[184:185], 0, s[28:29]
	s_mov_b32 m0, s0
	ds_read_b128 v[212:215], v199 offset:49152
	ds_read_b128 v[216:219], v199 offset:50176
	ds_read_b128 v[220:223], v199 offset:51200
	ds_read_b128 v[224:227], v199 offset:52224
	ds_read_b128 v[228:231], v199 offset:53248
	ds_read_b128 v[232:235], v199 offset:54272
	ds_read_b128 v[236:239], v199 offset:55296
	ds_read_b128 v[240:243], v199 offset:56320
	global_load_lds_dwordx4 v[184:185], off
	v_lshl_add_u64 v[184:185], v[186:187], 0, s[28:29]
	s_add_i32 m0, s0, 0x2000
	s_add_i32 s0, s50, s9
	global_load_lds_dwordx4 v[184:185], off
	v_lshl_add_u64 v[184:185], v[188:189], 0, s[28:29]
	s_mov_b32 m0, s0
	s_nop 0
	global_load_lds_dwordx4 v[184:185], off
	v_lshl_add_u64 v[184:185], v[190:191], 0, s[28:29]
	s_add_i32 m0, s0, 0x2000
	s_nop 0
	global_load_lds_dwordx4 v[184:185], off
	v_lshl_add_u64 v[184:185], v[192:193], 0, s[28:29]
	s_mov_b32 m0, s56
	s_nop 0
	global_load_lds_dwordx4 v[184:185], off
	v_lshl_add_u64 v[184:185], v[194:195], 0, s[28:29]
	s_mov_b32 m0, s57
	s_nop 0
	global_load_lds_dwordx4 v[184:185], off
	s_waitcnt vmcnt(6)
	s_waitcnt lgkmcnt(0)
	s_barrier
	s_setprio 1
	s_waitcnt lgkmcnt(0)
	v_mfma_scale_f32_16x16x128_f8f6f4 v[94:97], v[2:9], v[212:219], v[94:97], v200, v201 op_sel_hi:[0,0,0]
	v_mfma_scale_f32_16x16x128_f8f6f4 v[90:93], v[10:17], v[212:219], v[90:93], v200, v201 op_sel_hi:[0,0,0]
	v_mfma_scale_f32_16x16x128_f8f6f4 v[78:81], v[2:9], v[220:227], v[78:81], v200, v201 op_sel_hi:[0,0,0]
	v_mfma_scale_f32_16x16x128_f8f6f4 v[74:77], v[10:17], v[220:227], v[74:77], v200, v201 op_sel_hi:[0,0,0]
	v_mfma_scale_f32_16x16x128_f8f6f4 v[62:65], v[2:9], v[228:235], v[62:65], v200, v201 op_sel_hi:[0,0,0]
	v_mfma_scale_f32_16x16x128_f8f6f4 v[58:61], v[10:17], v[228:235], v[58:61], v200, v201 op_sel_hi:[0,0,0]
	v_mfma_scale_f32_16x16x128_f8f6f4 v[46:49], v[2:9], v[236:243], v[46:49], v200, v201 op_sel_hi:[0,0,0]
	v_mfma_scale_f32_16x16x128_f8f6f4 v[42:45], v[10:17], v[236:243], v[42:45], v200, v201 op_sel_hi:[0,0,0]
	s_setprio 0
	s_setprio 1
	v_mfma_scale_f32_16x16x128_f8f6f4 v[86:89], v[18:25], v[212:219], v[86:89], v200, v201 op_sel_hi:[0,0,0]
	v_mfma_scale_f32_16x16x128_f8f6f4 v[82:85], v[26:33], v[212:219], v[82:85], v200, v201 op_sel_hi:[0,0,0]
	v_mfma_scale_f32_16x16x128_f8f6f4 v[70:73], v[18:25], v[220:227], v[70:73], v200, v201 op_sel_hi:[0,0,0]
	v_mfma_scale_f32_16x16x128_f8f6f4 v[66:69], v[26:33], v[220:227], v[66:69], v200, v201 op_sel_hi:[0,0,0]
	v_mfma_scale_f32_16x16x128_f8f6f4 v[54:57], v[18:25], v[228:235], v[54:57], v200, v201 op_sel_hi:[0,0,0]
	v_mfma_scale_f32_16x16x128_f8f6f4 v[50:53], v[26:33], v[228:235], v[50:53], v200, v201 op_sel_hi:[0,0,0]
	v_mfma_scale_f32_16x16x128_f8f6f4 v[38:41], v[18:25], v[236:243], v[38:41], v200, v201 op_sel_hi:[0,0,0]
	v_mfma_scale_f32_16x16x128_f8f6f4 v[34:37], v[26:33], v[236:243], v[34:37], v200, v201 op_sel_hi:[0,0,0]
	s_setprio 0
	s_barrier
	s_add_u32 s46, s46, 0x100
	s_addc_u32 s47, s47, 0
	s_add_u32 s80, s80, 0x100
	s_addc_u32 s81, s81, 0
	s_cmp_ge_i32 s82, s58
	s_mov_b32 s48, s82
	s_cbranch_scc0 .LBB0_1625

; #define PG8_STAGE(bufoff, gbase, voff) do { _Pragma("unroll") for (int _i = 0; _i < 2; ++_i) \
;         __builtin_amdgcn_global_load_lds((const unsigned*)((const char*)(gbase) + (voff)[_i]), (PG8_LAS unsigned*)(lds + (bufoff) + ldsw + _i * 8192), 16, 0, 0); } while (0)
; #define PG8_LDA(dst, b, h) do { _Pragma("unroll") for (int m = 0; m < 4; ++m) { const bf16x8 f0_ = *(const PG8_LAS bf16x8*)(lds + PG8_SA(b, h) + aoff + m * 2048), f1_ = *(const PG8_LAS bf16x8*)(lds + PG8_SA(b, h) + aoff + m * 2048 + 1024); dst[m].set(f0_, f1_); } } while (0)
; #define PG8_LDB(dst, b, h) do { _Pragma("unroll") for (int n = 0; n < 2; ++n) { const bf16x8 f0_ = *(const PG8_LAS bf16x8*)(lds + PG8_SB(b, h) + boff + n * 2048), f1_ = *(const PG8_LAS bf16x8*)(lds + PG8_SB(b, h) + boff + n * 2048 + 1024); dst[n].set(f0_, f1_); } } while (0)
; #define PG8_WAIT_V(n) asm volatile("s_waitcnt vmcnt(" #n ")" ::: "memory")
; #define PG8_WAIT_L(n) asm volatile("s_waitcnt lgkmcnt(" #n ")" ::: "memory")
; #define PG8_BAR __builtin_amdgcn_s_barrier()
; #define PG8_SCHED __builtin_amdgcn_sched_barrier(0)
; template <class Epi, class Sched, bool ALIGN_EPI = false, bool SP2 = false>
; __device__ __forceinline__ void gemm_phase(PG8_LAS unsigned char* lds, const Gemm g, const Sched& S, const Epi& E) {
;     ...
;             const bool last = (t == nt - 2);
;             const char* a1 = cA + (size_t)(t + 1) * kstep;
;             const char* a2 = last ? nA : cA + (size_t)(t + 2) * kstep; const char* b2 = last ? nB : cB + (size_t)(t + 2) * kstep;
;             const char* a3 = a2 + kstep; const char* b3 = b2 + kstep;
;             if (last && has_next) S.a_ready(nxt);
;             if constexpr (SP2) {
;             PG8_LDB(B0, 0, 0); PG8_LDB(B1, 0, 1); PG8_SCHED; PG8_LDA(At, 0, 0); PG8_STAGE(PG8_SA(1, 1), a1 + hstep, voffA);
;             PG8_WAIT_V(8); PG8_WAIT_L(0); PG8_BAR; PG8_MMA(0, 0, At, B0); PG8_MMA(0, 1, At, B1); PG8_BAR; PG8_SCHED;
;             PG8_LDA(At, 0, 1); PG8_STAGE(PG8_SB(0, 0), b2, voffB); PG8_STAGE(PG8_SB(0, 1), b2 + hstepB, voffB); PG8_STAGE(PG8_SA(0, 0), a2, voffA);
;             PG8_WAIT_V(8); PG8_WAIT_L(0); PG8_BAR; PG8_MMA(1, 0, At, B0); PG8_MMA(1, 1, At, B1); PG8_BAR; PG8_SCHED;
.LBB0_1658:
	ds_read_b128 v[16:19], v215
	ds_read_b128 v[20:23], v215 offset:1024
	ds_read_b128 v[24:27], v215 offset:2048
	ds_read_b128 v[28:31], v215 offset:3072
	ds_read_b128 v[0:3], v216
	ds_read_b128 v[4:7], v216 offset:1024
	ds_read_b128 v[8:11], v216 offset:2048
	ds_read_b128 v[12:15], v216 offset:3072
	s_add_i32 s83, s78, 2
	s_add_u32 s0, s2, 0x80
	s_addc_u32 s1, s3, 0
	s_cmp_eq_u32 s97, s78
	s_cselect_b32 s78, s58, s0
	s_cselect_b32 s79, s59, s1
	s_cselect_b32 s81, s75, s82
	s_cselect_b32 s80, s74, s57
	v_lshl_add_u64 v[206:207], s[2:3], 0, v[198:199]
	s_add_i32 m0, s71, 0xc000
	ds_read_b128 v[152:155], v217
	ds_read_b128 v[156:159], v217 offset:1024
	ds_read_b128 v[168:171], v217 offset:2048
	ds_read_b128 v[172:175], v217 offset:3072
	ds_read_b128 v[176:179], v217 offset:4096
	ds_read_b128 v[180:183], v217 offset:5120
	ds_read_b128 v[226:229], v217 offset:6144
	ds_read_b128 v[230:233], v217 offset:7168
	global_load_lds_dwordx4 v[206:207], off
	v_lshl_add_u64 v[206:207], s[2:3], 0, v[200:201]
	s_add_i32 m0, s71, 0xe000
	s_nop 0
	global_load_lds_dwordx4 v[206:207], off
	s_waitcnt vmcnt(8)
	s_waitcnt lgkmcnt(0)
	s_barrier
	s_setprio 1
	s_waitcnt lgkmcnt(0)
	v_mfma_scale_f32_16x16x128_f8f6f4 v[164:167], v[16:23], v[152:159], v[164:167], v218, v219 op_sel_hi:[0,0,0]
	v_mfma_scale_f32_16x16x128_f8f6f4 v[160:163], v[24:31], v[152:159], v[160:163], v218, v219 op_sel_hi:[0,0,0]
	v_mfma_scale_f32_16x16x128_f8f6f4 v[140:143], v[16:23], v[168:175], v[140:143], v218, v219 op_sel_hi:[0,0,0]
	v_mfma_scale_f32_16x16x128_f8f6f4 v[136:139], v[24:31], v[168:175], v[136:139], v218, v219 op_sel_hi:[0,0,0]
	v_mfma_scale_f32_16x16x128_f8f6f4 v[108:111], v[16:23], v[176:183], v[108:111], v218, v219 op_sel_hi:[0,0,0]
	v_mfma_scale_f32_16x16x128_f8f6f4 v[104:107], v[24:31], v[176:183], v[104:107], v218, v219 op_sel_hi:[0,0,0]
	v_mfma_scale_f32_16x16x128_f8f6f4 v[116:119], v[16:23], v[226:233], v[116:119], v218, v219 op_sel_hi:[0,0,0]
	v_mfma_scale_f32_16x16x128_f8f6f4 v[112:115], v[24:31], v[226:233], v[112:115], v218, v219 op_sel_hi:[0,0,0]
	s_setprio 0
	s_setprio 1
	v_mfma_scale_f32_16x16x128_f8f6f4 v[148:151], v[0:7], v[152:159], v[148:151], v218, v219 op_sel_hi:[0,0,0]
	v_mfma_scale_f32_16x16x128_f8f6f4 v[144:147], v[8:15], v[152:159], v[144:147], v218, v219 op_sel_hi:[0,0,0]
	v_mfma_scale_f32_16x16x128_f8f6f4 v[132:135], v[0:7], v[168:175], v[132:135], v218, v219 op_sel_hi:[0,0,0]
	v_mfma_scale_f32_16x16x128_f8f6f4 v[128:131], v[8:15], v[168:175], v[128:131], v218, v219 op_sel_hi:[0,0,0]
	v_mfma_scale_f32_16x16x128_f8f6f4 v[124:127], v[0:7], v[176:183], v[124:127], v218, v219 op_sel_hi:[0,0,0]
	v_mfma_scale_f32_16x16x128_f8f6f4 v[120:123], v[8:15], v[176:183], v[120:123], v218, v219 op_sel_hi:[0,0,0]
	v_mfma_scale_f32_16x16x128_f8f6f4 v[100:103], v[0:7], v[226:233], v[100:103], v218, v219 op_sel_hi:[0,0,0]
	v_mfma_scale_f32_16x16x128_f8f6f4 v[96:99], v[8:15], v[226:233], v[96:99], v218, v219 op_sel_hi:[0,0,0]
	s_setprio 0
	s_barrier
	s_add_i32 s0, s67, s45
	v_lshl_add_u64 v[152:153], s[80:81], 0, v[186:187]
	s_mov_b32 m0, s0
	ds_read_b128 v[172:175], v217 offset:16384
	ds_read_b128 v[176:179], v217 offset:17408
	ds_read_b128 v[226:229], v217 offset:18432
	ds_read_b128 v[230:233], v217 offset:19456
	ds_read_b128 v[234:237], v217 offset:20480
	ds_read_b128 v[238:241], v217 offset:21504
	ds_read_b128 v[242:245], v217 offset:22528
	ds_read_b128 v[246:249], v217 offset:23552
	global_load_lds_dwordx4 v[152:153], off
	s_add_i32 m0, s0, 0x2000
	s_add_u32 s0, s80, s20
	v_lshl_add_u64 v[154:155], s[80:81], 0, v[190:191]
	s_addc_u32 s1, s81, s21
	s_add_i32 s33, s10, s45
	global_load_lds_dwordx4 v[154:155], off
	v_lshl_add_u64 v[156:157], s[0:1], 0, v[186:187]
	s_mov_b32 m0, s33
	v_lshl_add_u64 v[158:159], s[0:1], 0, v[190:191]
	global_load_lds_dwordx4 v[156:157], off
	s_add_i32 m0, s33, 0x2000
	v_lshl_add_u64 v[168:169], s[78:79], 0, v[184:185]
	global_load_lds_dwordx4 v[158:159], off
	v_lshl_add_u64 v[170:171], s[78:79], 0, v[188:189]
	s_waitcnt vmcnt(6)
	s_waitcnt lgkmcnt(0)
	s_barrier
	s_setprio 1
	s_waitcnt lgkmcnt(0)
	v_mfma_scale_f32_16x16x128_f8f6f4 v[92:95], v[16:23], v[172:179], v[92:95], v218, v219 op_sel_hi:[0,0,0]
	v_mfma_scale_f32_16x16x128_f8f6f4 v[88:91], v[24:31], v[172:179], v[88:91], v218, v219 op_sel_hi:[0,0,0]
	v_mfma_scale_f32_16x16x128_f8f6f4 v[76:79], v[16:23], v[226:233], v[76:79], v218, v219 op_sel_hi:[0,0,0]
	v_mfma_scale_f32_16x16x128_f8f6f4 v[72:75], v[24:31], v[226:233], v[72:75], v218, v219 op_sel_hi:[0,0,0]
	v_mfma_scale_f32_16x16x128_f8f6f4 v[60:63], v[16:23], v[234:241], v[60:63], v218, v219 op_sel_hi:[0,0,0]
	v_mfma_scale_f32_16x16x128_f8f6f4 v[56:59], v[24:31], v[234:241], v[56:59], v218, v219 op_sel_hi:[0,0,0]
	v_mfma_scale_f32_16x16x128_f8f6f4 v[44:47], v[16:23], v[242:249], v[44:47], v218, v219 op_sel_hi:[0,0,0]
	v_mfma_scale_f32_16x16x128_f8f6f4 v[40:43], v[24:31], v[242:249], v[40:43], v218, v219 op_sel_hi:[0,0,0]
	s_setprio 0
	s_setprio 1
	v_mfma_scale_f32_16x16x128_f8f6f4 v[84:87], v[0:7], v[172:179], v[84:87], v218, v219 op_sel_hi:[0,0,0]
	v_mfma_scale_f32_16x16x128_f8f6f4 v[80:83], v[8:15], v[172:179], v[80:83], v218, v219 op_sel_hi:[0,0,0]
	v_mfma_scale_f32_16x16x128_f8f6f4 v[68:71], v[0:7], v[226:233], v[68:71], v218, v219 op_sel_hi:[0,0,0]
	v_mfma_scale_f32_16x16x128_f8f6f4 v[64:67], v[8:15], v[226:233], v[64:67], v218, v219 op_sel_hi:[0,0,0]
	v_mfma_scale_f32_16x16x128_f8f6f4 v[52:55], v[0:7], v[234:241], v[52:55], v218, v219 op_sel_hi:[0,0,0]
	v_mfma_scale_f32_16x16x128_f8f6f4 v[48:51], v[8:15], v[234:241], v[48:51], v218, v219 op_sel_hi:[0,0,0]
	v_mfma_scale_f32_16x16x128_f8f6f4 v[36:39], v[0:7], v[242:249], v[36:39], v218, v219 op_sel_hi:[0,0,0]
	v_mfma_scale_f32_16x16x128_f8f6f4 v[32:35], v[8:15], v[242:249], v[32:35], v218, v219 op_sel_hi:[0,0,0]
	s_setprio 0
	s_barrier
; #define PG8_STAGE(bufoff, gbase, voff) do { _Pragma("unroll") for (int _i = 0; _i < 2; ++_i) \
;         __builtin_amdgcn_global_load_lds((const unsigned*)((const char*)(gbase) + (voff)[_i]), (PG8_LAS unsigned*)(lds + (bufoff) + ldsw + _i * 8192), 16, 0, 0); } while (0)
; #define PG8_LDA(dst, b, h) do { _Pragma("unroll") for (int m = 0; m < 4; ++m) { const bf16x8 f0_ = *(const PG8_LAS bf16x8*)(lds + PG8_SA(b, h) + aoff + m * 2048), f1_ = *(const PG8_LAS bf16x8*)(lds + PG8_SA(b, h) + aoff + m * 2048 + 1024); dst[m].set(f0_, f1_); } } while (0)
; #define PG8_LDB(dst, b, h) do { _Pragma("unroll") for (int n = 0; n < 2; ++n) { const bf16x8 f0_ = *(const PG8_LAS bf16x8*)(lds + PG8_SB(b, h) + boff + n * 2048), f1_ = *(const PG8_LAS bf16x8*)(lds + PG8_SB(b, h) + boff + n * 2048 + 1024); dst[n].set(f0_, f1_); } } while (0)
; #define PG8_WAIT_V(n) asm volatile("s_waitcnt vmcnt(" #n ")" ::: "memory")
; #define PG8_WAIT_L(n) asm volatile("s_waitcnt lgkmcnt(" #n ")" ::: "memory")
; #define PG8_BAR __builtin_amdgcn_s_barrier()
; #define PG8_SCHED __builtin_amdgcn_sched_barrier(0)
; template <class Epi, class Sched, bool ALIGN_EPI = false, bool SP2 = false>
; __device__ __forceinline__ void gemm_phase(PG8_LAS unsigned char* lds, const Gemm g, const Sched& S, const Epi& E) {
;     ...
;             PG8_LDB(B0, 1, 0); PG8_LDB(B1, 1, 1); PG8_SCHED; PG8_LDA(At, 1, 0); PG8_STAGE(PG8_SA(0, 1), a2 + hstep, voffA);
;             PG8_WAIT_V(8); PG8_WAIT_L(0); PG8_BAR; PG8_MMA(0, 0, At, B0); PG8_MMA(0, 1, At, B1); PG8_BAR; PG8_SCHED;
;             PG8_LDA(At, 1, 1); PG8_STAGE(PG8_SB(1, 0), b3, voffB); PG8_STAGE(PG8_SB(1, 1), b3 + hstepB, voffB); PG8_STAGE(PG8_SA(1, 0), a3, voffA);
;             PG8_WAIT_V(8); PG8_WAIT_L(0); PG8_BAR; PG8_MMA(1, 0, At, B0); PG8_MMA(1, 1, At, B1); PG8_BAR; PG8_SCHED;
	s_add_i32 s33, 0, 0x18000
	s_add_i32 s80, 0, 0x1c000
	v_add_u32_e32 v12, s33, v211
	v_add_u32_e32 v28, s80, v211
	ds_read_b128 v[0:3], v12
	ds_read_b128 v[4:7], v12 offset:1024
	ds_read_b128 v[8:11], v12 offset:2048
	ds_read_b128 v[12:15], v12 offset:3072
	ds_read_b128 v[16:19], v28
	ds_read_b128 v[20:23], v28 offset:1024
	ds_read_b128 v[24:27], v28 offset:2048
	ds_read_b128 v[28:31], v28 offset:3072
	s_add_u32 s0, s78, s18
	s_addc_u32 s1, s79, s19
	s_mov_b32 m0, s86
	v_lshl_add_u64 v[180:181], s[0:1], 0, v[184:185]
	ds_read_b128 v[172:175], v217 offset:32768
	ds_read_b128 v[176:179], v217 offset:33792
	ds_read_b128 v[226:229], v217 offset:34816
	ds_read_b128 v[230:233], v217 offset:35840
	ds_read_b128 v[234:237], v217 offset:36864
	ds_read_b128 v[238:241], v217 offset:37888
	ds_read_b128 v[242:245], v217 offset:38912
	ds_read_b128 v[246:249], v217 offset:39936
	global_load_lds_dwordx4 v[180:181], off
	v_lshl_add_u64 v[180:181], s[0:1], 0, v[188:189]
	s_mov_b32 m0, s87
	s_nop 0
	global_load_lds_dwordx4 v[180:181], off
	s_mov_b32 m0, s71
	s_nop 0
	global_load_lds_dwordx4 v[168:169], off
	s_mov_b32 m0, s73
	s_nop 0
	global_load_lds_dwordx4 v[170:171], off
	s_waitcnt vmcnt(8)
	s_waitcnt lgkmcnt(0)
	s_barrier
	s_setprio 1
	s_waitcnt lgkmcnt(0)
	v_mfma_scale_f32_16x16x128_f8f6f4 v[164:167], v[0:7], v[172:179], v[164:167], v218, v219 op_sel_hi:[0,0,0]
	v_mfma_scale_f32_16x16x128_f8f6f4 v[160:163], v[8:15], v[172:179], v[160:163], v218, v219 op_sel_hi:[0,0,0]
	v_mfma_scale_f32_16x16x128_f8f6f4 v[140:143], v[0:7], v[226:233], v[140:143], v218, v219 op_sel_hi:[0,0,0]
	v_mfma_scale_f32_16x16x128_f8f6f4 v[136:139], v[8:15], v[226:233], v[136:139], v218, v219 op_sel_hi:[0,0,0]
	v_mfma_scale_f32_16x16x128_f8f6f4 v[108:111], v[0:7], v[234:241], v[108:111], v218, v219 op_sel_hi:[0,0,0]
	v_mfma_scale_f32_16x16x128_f8f6f4 v[104:107], v[8:15], v[234:241], v[104:107], v218, v219 op_sel_hi:[0,0,0]
	v_mfma_scale_f32_16x16x128_f8f6f4 v[116:119], v[0:7], v[242:249], v[116:119], v218, v219 op_sel_hi:[0,0,0]
	v_mfma_scale_f32_16x16x128_f8f6f4 v[112:115], v[8:15], v[242:249], v[112:115], v218, v219 op_sel_hi:[0,0,0]
	s_setprio 0
	s_setprio 1
	v_mfma_scale_f32_16x16x128_f8f6f4 v[148:151], v[16:23], v[172:179], v[148:151], v218, v219 op_sel_hi:[0,0,0]
	v_mfma_scale_f32_16x16x128_f8f6f4 v[144:147], v[24:31], v[172:179], v[144:147], v218, v219 op_sel_hi:[0,0,0]
	v_mfma_scale_f32_16x16x128_f8f6f4 v[132:135], v[16:23], v[226:233], v[132:135], v218, v219 op_sel_hi:[0,0,0]
	v_mfma_scale_f32_16x16x128_f8f6f4 v[128:131], v[24:31], v[226:233], v[128:131], v218, v219 op_sel_hi:[0,0,0]
	v_mfma_scale_f32_16x16x128_f8f6f4 v[124:127], v[16:23], v[234:241], v[124:127], v218, v219 op_sel_hi:[0,0,0]
	v_mfma_scale_f32_16x16x128_f8f6f4 v[120:123], v[24:31], v[234:241], v[120:123], v218, v219 op_sel_hi:[0,0,0]
	v_mfma_scale_f32_16x16x128_f8f6f4 v[100:103], v[16:23], v[242:249], v[100:103], v218, v219 op_sel_hi:[0,0,0]
	v_mfma_scale_f32_16x16x128_f8f6f4 v[96:99], v[24:31], v[242:249], v[96:99], v218, v219 op_sel_hi:[0,0,0]
	s_setprio 0
	s_barrier
	s_add_i32 s0, s33, s45
	v_lshl_add_u64 v[152:153], v[152:153], 0, s[36:37]
	s_mov_b32 m0, s0
	ds_read_b128 v[172:175], v217 offset:49152
	ds_read_b128 v[176:179], v217 offset:50176
	ds_read_b128 v[226:229], v217 offset:51200
	ds_read_b128 v[230:233], v217 offset:52224
	ds_read_b128 v[234:237], v217 offset:53248
	ds_read_b128 v[238:241], v217 offset:54272
	ds_read_b128 v[242:245], v217 offset:55296
	ds_read_b128 v[246:249], v217 offset:56320
	global_load_lds_dwordx4 v[152:153], off
	v_lshl_add_u64 v[152:153], v[154:155], 0, s[36:37]
	s_add_i32 m0, s0, 0x2000
	s_add_i32 s0, s80, s45
	global_load_lds_dwordx4 v[152:153], off
	v_lshl_add_u64 v[152:153], v[156:157], 0, s[36:37]
	s_mov_b32 m0, s0
	s_nop 0
	global_load_lds_dwordx4 v[152:153], off
	v_lshl_add_u64 v[152:153], v[158:159], 0, s[36:37]
	s_add_i32 m0, s0, 0x2000
	s_nop 0
	global_load_lds_dwordx4 v[152:153], off
	v_lshl_add_u64 v[152:153], v[168:169], 0, s[36:37]
	s_mov_b32 m0, s93
	s_nop 0
	global_load_lds_dwordx4 v[152:153], off
	v_lshl_add_u64 v[152:153], v[170:171], 0, s[36:37]
	s_mov_b32 m0, s94
	s_nop 0
	global_load_lds_dwordx4 v[152:153], off
	s_waitcnt vmcnt(6)
	s_waitcnt lgkmcnt(0)
	s_barrier
	s_setprio 1
	s_waitcnt lgkmcnt(0)
	v_mfma_scale_f32_16x16x128_f8f6f4 v[92:95], v[0:7], v[172:179], v[92:95], v218, v219 op_sel_hi:[0,0,0]
	v_mfma_scale_f32_16x16x128_f8f6f4 v[88:91], v[8:15], v[172:179], v[88:91], v218, v219 op_sel_hi:[0,0,0]
	v_mfma_scale_f32_16x16x128_f8f6f4 v[76:79], v[0:7], v[226:233], v[76:79], v218, v219 op_sel_hi:[0,0,0]
	v_mfma_scale_f32_16x16x128_f8f6f4 v[72:75], v[8:15], v[226:233], v[72:75], v218, v219 op_sel_hi:[0,0,0]
	v_mfma_scale_f32_16x16x128_f8f6f4 v[60:63], v[0:7], v[234:241], v[60:63], v218, v219 op_sel_hi:[0,0,0]
	v_mfma_scale_f32_16x16x128_f8f6f4 v[56:59], v[8:15], v[234:241], v[56:59], v218, v219 op_sel_hi:[0,0,0]
	v_mfma_scale_f32_16x16x128_f8f6f4 v[44:47], v[0:7], v[242:249], v[44:47], v218, v219 op_sel_hi:[0,0,0]
	v_mfma_scale_f32_16x16x128_f8f6f4 v[40:43], v[8:15], v[242:249], v[40:43], v218, v219 op_sel_hi:[0,0,0]
	s_setprio 0
	s_setprio 1
	v_mfma_scale_f32_16x16x128_f8f6f4 v[84:87], v[16:23], v[172:179], v[84:87], v218, v219 op_sel_hi:[0,0,0]
	v_mfma_scale_f32_16x16x128_f8f6f4 v[80:83], v[24:31], v[172:179], v[80:83], v218, v219 op_sel_hi:[0,0,0]
	v_mfma_scale_f32_16x16x128_f8f6f4 v[68:71], v[16:23], v[226:233], v[68:71], v218, v219 op_sel_hi:[0,0,0]
	v_mfma_scale_f32_16x16x128_f8f6f4 v[64:67], v[24:31], v[226:233], v[64:67], v218, v219 op_sel_hi:[0,0,0]
	v_mfma_scale_f32_16x16x128_f8f6f4 v[52:55], v[16:23], v[234:241], v[52:55], v218, v219 op_sel_hi:[0,0,0]
	v_mfma_scale_f32_16x16x128_f8f6f4 v[48:51], v[24:31], v[234:241], v[48:51], v218, v219 op_sel_hi:[0,0,0]
	v_mfma_scale_f32_16x16x128_f8f6f4 v[36:39], v[16:23], v[242:249], v[36:39], v218, v219 op_sel_hi:[0,0,0]
	v_mfma_scale_f32_16x16x128_f8f6f4 v[32:35], v[24:31], v[242:249], v[32:35], v218, v219 op_sel_hi:[0,0,0]
	s_setprio 0
	s_barrier
	s_add_u32 s2, s2, 0x100
	s_addc_u32 s3, s3, 0
	s_add_u32 s57, s57, 0x100
	s_addc_u32 s82, s82, 0
	s_cmp_ge_i32 s83, s91
	s_mov_b32 s78, s83
	s_cbranch_scc0 .LBB0_1658
